# v049 with the leading half's epilogue priority dropped back to 0 after half of the epilogue stores
# speedup vs baseline: 1.0142x; 1.0090x over previous
.LBB0_288:
	v_lshl_add_u32 v8, s68, 8, v182
	v_lshl_or_b32 v2, s2, 8, v184
	v_ashrrev_i32_e32 v9, 31, v8
	v_ashrrev_i32_e32 v3, 31, v2
	v_lshlrev_b64 v[4:5], 13, v[8:9]
	v_lshl_add_u64 v[4:5], s[6:7], 0, v[4:5]
	v_lshlrev_b64 v[10:11], 1, v[2:3]
	s_nop 15
	s_nop 15
	v_lshl_add_u64 v[2:3], v[4:5], 0, v[10:11]
	v_cvt_pk_bf16_f32 v4, v158, v159
	v_cvt_pk_bf16_f32 v5, v160, v161
	v_cvt_pk_bf16_f32 v6, v154, v155
	v_cvt_pk_bf16_f32 v7, v156, v157
	global_store_dwordx4 v[2:3], v[4:7], off
	s_mov_b32 s2, 0x100000
	s_mov_b64 s[26:27], 0x100000
	v_cvt_pk_bf16_f32 v4, v146, v147
	v_cvt_pk_bf16_f32 v5, v148, v149
	v_cvt_pk_bf16_f32 v6, v138, v139
	v_cvt_pk_bf16_f32 v7, v140, v141
	global_store_dwordx4 v[2:3], v[4:7], off offset:256
	v_readlane_b32 s96, v254, 60
	v_readlane_b32 s97, v254, 61
	v_or_b32_e32 v4, 16, v8
	v_ashrrev_i32_e32 v5, 31, v4
	v_lshlrev_b64 v[4:5], 13, v[4:5]
	v_lshl_add_u64 v[4:5], s[6:7], 0, v[4:5]
	v_lshl_add_u64 v[12:13], v[4:5], 0, v[10:11]
	v_cvt_pk_bf16_f32 v4, v150, v151
	v_cvt_pk_bf16_f32 v5, v152, v153
	v_cvt_pk_bf16_f32 v6, v142, v143
	v_cvt_pk_bf16_f32 v7, v144, v145
	global_store_dwordx4 v[12:13], v[4:7], off
	s_nop 1
	v_cvt_pk_bf16_f32 v4, v130, v131
	v_cvt_pk_bf16_f32 v5, v132, v133
	v_cvt_pk_bf16_f32 v6, v122, v123
	v_cvt_pk_bf16_f32 v7, v124, v125
	global_store_dwordx4 v[12:13], v[4:7], off offset:256
	s_nop 1
	v_or_b32_e32 v4, 32, v8
	v_ashrrev_i32_e32 v5, 31, v4
	v_lshlrev_b64 v[4:5], 13, v[4:5]
	v_lshl_add_u64 v[4:5], s[6:7], 0, v[4:5]
	v_lshl_add_u64 v[12:13], v[4:5], 0, v[10:11]
	v_cvt_pk_bf16_f32 v4, v134, v135
	v_cvt_pk_bf16_f32 v5, v136, v137
	v_cvt_pk_bf16_f32 v6, v126, v127
	v_cvt_pk_bf16_f32 v7, v128, v129
	global_store_dwordx4 v[12:13], v[4:7], off
	s_nop 1
	v_cvt_pk_bf16_f32 v4, v114, v115
	v_cvt_pk_bf16_f32 v5, v116, v117
	v_cvt_pk_bf16_f32 v6, v106, v107
	v_cvt_pk_bf16_f32 v7, v108, v109
	global_store_dwordx4 v[12:13], v[4:7], off offset:256
	s_nop 1
	v_or_b32_e32 v4, 48, v8
	v_ashrrev_i32_e32 v5, 31, v4
	v_lshlrev_b64 v[4:5], 13, v[4:5]
	v_lshl_add_u64 v[4:5], s[6:7], 0, v[4:5]
	v_lshl_add_u64 v[8:9], v[4:5], 0, v[10:11]
	v_cvt_pk_bf16_f32 v4, v118, v119
	v_cvt_pk_bf16_f32 v5, v120, v121
	v_cvt_pk_bf16_f32 v6, v110, v111
	v_cvt_pk_bf16_f32 v7, v112, v113
	global_store_dwordx4 v[8:9], v[4:7], off
	v_add_co_u32_e32 v10, vcc, s2, v2
	s_nop 0
	v_cvt_pk_bf16_f32 v4, v102, v103
	v_cvt_pk_bf16_f32 v5, v104, v105
	v_cvt_pk_bf16_f32 v6, v98, v99
	v_cvt_pk_bf16_f32 v7, v100, v101
	global_store_dwordx4 v[8:9], v[4:7], off offset:256
	s_setprio 0
	v_addc_co_u32_e32 v11, vcc, 0, v3, vcc
	s_nop 0
	v_cvt_pk_bf16_f32 v4, v94, v95
	v_cvt_pk_bf16_f32 v5, v96, v97
	v_cvt_pk_bf16_f32 v6, v90, v91
	v_cvt_pk_bf16_f32 v7, v92, v93
	s_mov_b32 s2, 0x120000
	v_lshl_add_u64 v[8:9], v[2:3], 0, s[26:27]
	global_store_dwordx4 v[10:11], v[4:7], off
	v_add_co_u32_e32 v10, vcc, s2, v2
	s_nop 0
	v_cvt_pk_bf16_f32 v4, v82, v83
	v_cvt_pk_bf16_f32 v5, v84, v85
	v_cvt_pk_bf16_f32 v6, v74, v75
	v_cvt_pk_bf16_f32 v7, v76, v77
	global_store_dwordx4 v[8:9], v[4:7], off offset:256
	s_mov_b64 s[26:27], 0x120000
	v_addc_co_u32_e32 v11, vcc, 0, v3, vcc
	v_cvt_pk_bf16_f32 v4, v86, v87
	v_cvt_pk_bf16_f32 v5, v88, v89
	v_cvt_pk_bf16_f32 v6, v78, v79
	v_cvt_pk_bf16_f32 v7, v80, v81
	s_mov_b32 s2, 0x140000
	v_lshl_add_u64 v[8:9], v[2:3], 0, s[26:27]
	global_store_dwordx4 v[10:11], v[4:7], off
	s_mov_b64 s[26:27], 0x140000
	v_add_co_u32_e32 v10, vcc, s2, v2
	v_cvt_pk_bf16_f32 v4, v66, v67
	v_cvt_pk_bf16_f32 v5, v68, v69
	v_cvt_pk_bf16_f32 v6, v58, v59
	v_cvt_pk_bf16_f32 v7, v60, v61
	global_store_dwordx4 v[8:9], v[4:7], off offset:256
	v_lshl_add_u64 v[8:9], v[2:3], 0, s[26:27]
	v_addc_co_u32_e32 v11, vcc, 0, v3, vcc
	v_cvt_pk_bf16_f32 v4, v70, v71
	v_cvt_pk_bf16_f32 v5, v72, v73
	v_cvt_pk_bf16_f32 v6, v62, v63
	v_cvt_pk_bf16_f32 v7, v64, v65
	s_mov_b64 s[26:27], 0x160000
	s_mov_b32 s2, 0x160000
	global_store_dwordx4 v[10:11], v[4:7], off
	s_nop 1
	v_cvt_pk_bf16_f32 v4, v50, v51
	v_cvt_pk_bf16_f32 v5, v52, v53
	v_cvt_pk_bf16_f32 v6, v42, v43
	v_cvt_pk_bf16_f32 v7, v44, v45
	global_store_dwordx4 v[8:9], v[4:7], off offset:256
	v_lshl_add_u64 v[8:9], v[2:3], 0, s[26:27]
	v_add_co_u32_e32 v2, vcc, s2, v2
	v_cvt_pk_bf16_f32 v4, v54, v55
	v_cvt_pk_bf16_f32 v5, v56, v57
	v_cvt_pk_bf16_f32 v6, v46, v47
	v_cvt_pk_bf16_f32 v7, v48, v49
	s_nop 1
	v_addc_co_u32_e32 v3, vcc, 0, v3, vcc
	s_andn2_b64 vcc, exec, s[0:1]
	s_mov_b64 s[0:1], -1
	global_store_dwordx4 v[2:3], v[4:7], off
	v_cvt_pk_bf16_f32 v2, v38, v39
	v_cvt_pk_bf16_f32 v3, v40, v41
	s_nop 1
	v_cvt_pk_bf16_f32 v4, v34, v35
	v_cvt_pk_bf16_f32 v5, v36, v37
	global_store_dwordx4 v[8:9], v[2:5], off offset:256
	s_cbranch_vccnz .LBB0_277
	s_andn2_b64 vcc, exec, s[14:15]
	s_cbranch_vccnz .LBB0_276
	s_barrier
	s_branch .LBB0_276

.LBB0_663:
	v_lshl_or_b32 v132, s2, 8, v221
	v_lshl_add_u32 v130, s56, 8, v219
	v_ashrrev_i32_e32 v133, 31, v132
	v_readlane_b32 s80, v254, 7
	v_lshlrev_b64 v[208:209], 2, v[132:133]
	v_readlane_b32 s81, v254, 8
	v_ashrrev_i32_e32 v131, 31, v130
	v_lshlrev_b64 v[212:213], 13, v[130:131]
	v_lshl_add_u64 v[210:211], s[80:81], 0, v[208:209]
	v_lshl_add_u64 v[132:133], v[210:211], 0, v[212:213]
	global_load_dwordx4 v[158:161], v[132:133], off
	global_load_dwordx4 v[150:153], v[132:133], off offset:64
	global_load_dwordx4 v[146:149], v[132:133], off offset:512
	global_load_dwordx4 v[142:145], v[132:133], off offset:576
	v_or_b32_e32 v132, 16, v130
	v_ashrrev_i32_e32 v133, 31, v132
	v_lshlrev_b64 v[226:227], 13, v[132:133]
	v_lshl_add_u64 v[132:133], v[210:211], 0, v[226:227]
	global_load_dwordx4 v[174:177], v[132:133], off
	global_load_dwordx4 v[166:169], v[132:133], off offset:64
	global_load_dwordx4 v[162:165], v[132:133], off offset:512
	global_load_dwordx4 v[154:157], v[132:133], off offset:576
	v_or_b32_e32 v132, 32, v130
	v_or_b32_e32 v130, 48, v130
	v_ashrrev_i32_e32 v133, 31, v132
	v_ashrrev_i32_e32 v131, 31, v130
	v_lshlrev_b64 v[228:229], 13, v[132:133]
	v_lshlrev_b64 v[216:217], 13, v[130:131]
	v_lshl_add_u64 v[132:133], v[210:211], 0, v[228:229]
	v_lshl_add_u64 v[130:131], v[210:211], 0, v[216:217]
	global_load_dwordx4 v[186:189], v[132:133], off
	global_load_dwordx4 v[182:185], v[132:133], off offset:64
	global_load_dwordx4 v[178:181], v[132:133], off offset:512
	global_load_dwordx4 v[170:173], v[132:133], off offset:576
	global_load_dwordx4 v[190:193], v[130:131], off
	global_load_dwordx4 v[138:141], v[130:131], off offset:64
	global_load_dwordx4 v[134:137], v[130:131], off offset:512
	s_nop 0
	global_load_dwordx4 v[130:133], v[130:131], off offset:576
	v_lshl_add_u64 v[214:215], s[78:79], 0, v[212:213]
	v_lshl_add_u64 v[216:217], s[78:79], 0, v[216:217]
	s_mov_b64 s[26:27], 0x100000
	v_lshl_add_u64 v[214:215], v[214:215], 0, v[208:209]
	v_lshl_add_u64 v[226:227], s[78:79], 0, v[226:227]
	v_lshl_add_u64 v[228:229], s[78:79], 0, v[228:229]
	v_lshl_add_u64 v[216:217], v[216:217], 0, v[208:209]
	v_lshl_add_u64 v[226:227], v[226:227], 0, v[208:209]
	v_lshl_add_u64 v[228:229], v[228:229], 0, v[208:209]
	s_andn2_b64 vcc, exec, s[0:1]
	s_mov_b64 s[0:1], -1
	v_readlane_b32 s82, v254, 9
	v_readlane_b32 s83, v254, 10
	v_readlane_b32 s84, v254, 11
	v_readlane_b32 s85, v254, 12
	v_readlane_b32 s86, v254, 13
	v_readlane_b32 s87, v254, 14
	v_readlane_b32 s88, v254, 15
	v_readlane_b32 s89, v254, 16
	v_readlane_b32 s90, v254, 17
	v_readlane_b32 s91, v254, 18
	v_readlane_b32 s92, v254, 19
	v_readlane_b32 s93, v254, 20
	v_readlane_b32 s94, v254, 21
	v_readlane_b32 s95, v254, 22
	s_waitcnt vmcnt(0)
	v_pk_add_f32 v[128:129], v[128:129], v[160:161]
	v_pk_add_f32 v[126:127], v[126:127], v[158:159]
	v_pk_add_f32 v[124:125], v[124:125], v[152:153]
	v_pk_add_f32 v[122:123], v[122:123], v[150:151]
	v_pk_add_f32 v[108:109], v[108:109], v[148:149]
	v_pk_add_f32 v[106:107], v[106:107], v[146:147]
	v_pk_add_f32 v[100:101], v[100:101], v[144:145]
	v_pk_add_f32 v[98:99], v[98:99], v[142:143]
	v_pk_add_f32 v[120:121], v[120:121], v[176:177]
	v_pk_add_f32 v[118:119], v[118:119], v[174:175]
	v_pk_add_f32 v[116:117], v[116:117], v[168:169]
	v_pk_add_f32 v[114:115], v[114:115], v[166:167]
	v_pk_add_f32 v[92:93], v[92:93], v[164:165]
	v_pk_add_f32 v[90:91], v[90:91], v[162:163]
	v_pk_add_f32 v[88:89], v[88:89], v[156:157]
	v_pk_add_f32 v[86:87], v[86:87], v[154:155]
	v_pk_add_f32 v[112:113], v[112:113], v[188:189]
	v_pk_add_f32 v[72:73], v[72:73], v[136:137]
	v_pk_add_f32 v[70:71], v[70:71], v[134:135]
	v_pk_add_f32 v[68:69], v[68:69], v[132:133]
	v_pk_add_f32 v[66:67], v[66:67], v[130:131]
	v_lshl_add_u64 v[132:133], v[212:213], 0, s[26:27]
	s_mov_b64 s[26:27], 0x120000
	v_pk_add_f32 v[110:111], v[110:111], v[186:187]
	v_pk_add_f32 v[104:105], v[104:105], v[184:185]
	v_pk_add_f32 v[102:103], v[102:103], v[182:183]
	v_pk_add_f32 v[84:85], v[84:85], v[180:181]
	v_pk_add_f32 v[82:83], v[82:83], v[178:179]
	v_pk_add_f32 v[80:81], v[80:81], v[172:173]
	v_pk_add_f32 v[78:79], v[78:79], v[170:171]
	v_pk_add_f32 v[96:97], v[96:97], v[192:193]
	v_pk_add_f32 v[94:95], v[94:95], v[190:191]
	v_pk_add_f32 v[76:77], v[76:77], v[140:141]
	v_pk_add_f32 v[74:75], v[74:75], v[138:139]
	global_store_dwordx4 v[214:215], v[126:129], off
	global_store_dwordx4 v[214:215], v[122:125], off offset:64
	global_store_dwordx4 v[214:215], v[106:109], off offset:512
	global_store_dwordx4 v[214:215], v[98:101], off offset:576
	global_store_dwordx4 v[226:227], v[118:121], off
	global_store_dwordx4 v[226:227], v[114:117], off offset:64
	global_store_dwordx4 v[226:227], v[90:93], off offset:512
	global_store_dwordx4 v[226:227], v[86:89], off offset:576
	global_store_dwordx4 v[228:229], v[110:113], off
	global_store_dwordx4 v[228:229], v[102:105], off offset:64
	global_store_dwordx4 v[228:229], v[82:85], off offset:512
	global_store_dwordx4 v[228:229], v[78:81], off offset:576
	global_store_dwordx4 v[216:217], v[94:97], off
	global_store_dwordx4 v[216:217], v[74:77], off offset:64
	global_store_dwordx4 v[216:217], v[70:73], off offset:512
	global_store_dwordx4 v[216:217], v[66:69], off offset:576
	s_setprio 0
	v_lshl_add_u64 v[134:135], v[212:213], 0, s[26:27]
	s_mov_b64 s[26:27], 0x140000
	v_lshl_add_u64 v[66:67], v[210:211], 0, v[132:133]
	global_load_dwordx4 v[126:129], v[66:67], off
	global_load_dwordx4 v[118:121], v[66:67], off offset:64
	global_load_dwordx4 v[106:109], v[66:67], off offset:512
	global_load_dwordx4 v[90:93], v[66:67], off offset:576
	v_lshl_add_u64 v[66:67], v[210:211], 0, v[134:135]
	v_lshl_add_u64 v[136:137], v[212:213], 0, s[26:27]
	s_mov_b64 s[26:27], 0x160000
	global_load_dwordx4 v[122:125], v[66:67], off
	global_load_dwordx4 v[110:113], v[66:67], off offset:64
	global_load_dwordx4 v[94:97], v[66:67], off offset:512
	global_load_dwordx4 v[82:85], v[66:67], off offset:576
	v_lshl_add_u64 v[66:67], v[210:211], 0, v[136:137]
	v_lshl_add_u64 v[130:131], v[212:213], 0, s[26:27]
	global_load_dwordx4 v[114:117], v[66:67], off
	global_load_dwordx4 v[98:101], v[66:67], off offset:64
	global_load_dwordx4 v[86:89], v[66:67], off offset:512
	global_load_dwordx4 v[78:81], v[66:67], off offset:576
	v_lshl_add_u64 v[66:67], v[210:211], 0, v[130:131]
	global_load_dwordx4 v[102:105], v[66:67], off
	global_load_dwordx4 v[74:77], v[66:67], off offset:64
	global_load_dwordx4 v[70:73], v[66:67], off offset:512
	s_nop 0
	global_load_dwordx4 v[66:69], v[66:67], off offset:576
	v_lshl_add_u64 v[132:133], s[78:79], 0, v[132:133]
	v_lshl_add_u64 v[134:135], s[78:79], 0, v[134:135]
	v_lshl_add_u64 v[136:137], s[78:79], 0, v[136:137]
	v_lshl_add_u64 v[130:131], s[78:79], 0, v[130:131]
	v_lshl_add_u64 v[132:133], v[132:133], 0, v[208:209]
	v_lshl_add_u64 v[134:135], v[134:135], 0, v[208:209]
	v_lshl_add_u64 v[136:137], v[136:137], 0, v[208:209]
	s_waitcnt vmcnt(15)
	v_pk_add_f32 v[64:65], v[64:65], v[128:129]
	v_pk_add_f32 v[62:63], v[62:63], v[126:127]
	s_waitcnt vmcnt(14)
	v_pk_add_f32 v[60:61], v[60:61], v[120:121]
	v_pk_add_f32 v[58:59], v[58:59], v[118:119]
	s_waitcnt vmcnt(13)
	v_pk_add_f32 v[44:45], v[44:45], v[108:109]
	v_pk_add_f32 v[42:43], v[42:43], v[106:107]
	s_waitcnt vmcnt(12)
	v_pk_add_f32 v[36:37], v[36:37], v[92:93]
	v_pk_add_f32 v[34:35], v[34:35], v[90:91]
	s_waitcnt vmcnt(11)
	v_pk_add_f32 v[56:57], v[56:57], v[124:125]
	v_pk_add_f32 v[54:55], v[54:55], v[122:123]
	s_waitcnt vmcnt(4)
	v_pk_add_f32 v[14:15], v[14:15], v[78:79]
	v_pk_add_f32 v[52:53], v[52:53], v[112:113]
	v_pk_add_f32 v[50:51], v[50:51], v[110:111]
	v_pk_add_f32 v[28:29], v[28:29], v[96:97]
	v_pk_add_f32 v[26:27], v[26:27], v[94:95]
	v_pk_add_f32 v[24:25], v[24:25], v[84:85]
	v_pk_add_f32 v[22:23], v[22:23], v[82:83]
	v_pk_add_f32 v[48:49], v[48:49], v[116:117]
	v_pk_add_f32 v[46:47], v[46:47], v[114:115]
	v_pk_add_f32 v[40:41], v[40:41], v[100:101]
	v_pk_add_f32 v[38:39], v[38:39], v[98:99]
	v_pk_add_f32 v[20:21], v[20:21], v[88:89]
	v_pk_add_f32 v[18:19], v[18:19], v[86:87]
	v_pk_add_f32 v[16:17], v[16:17], v[80:81]
	s_waitcnt vmcnt(3)
	v_pk_add_f32 v[32:33], v[32:33], v[104:105]
	v_pk_add_f32 v[30:31], v[30:31], v[102:103]
	global_store_dwordx4 v[132:133], v[62:65], off
	global_store_dwordx4 v[132:133], v[58:61], off offset:64
	global_store_dwordx4 v[132:133], v[42:45], off offset:512
	global_store_dwordx4 v[132:133], v[34:37], off offset:576
	global_store_dwordx4 v[134:135], v[54:57], off
	global_store_dwordx4 v[134:135], v[50:53], off offset:64
	global_store_dwordx4 v[134:135], v[26:29], off offset:512
	global_store_dwordx4 v[134:135], v[22:25], off offset:576
	global_store_dwordx4 v[136:137], v[46:49], off
	global_store_dwordx4 v[136:137], v[38:41], off offset:64
	global_store_dwordx4 v[136:137], v[18:21], off offset:512
	global_store_dwordx4 v[136:137], v[14:17], off offset:576
	s_waitcnt vmcnt(14)
	v_pk_add_f32 v[12:13], v[12:13], v[76:77]
	v_pk_add_f32 v[10:11], v[10:11], v[74:75]
	v_lshl_add_u64 v[14:15], v[130:131], 0, v[208:209]
	s_waitcnt vmcnt(13)
	v_pk_add_f32 v[8:9], v[8:9], v[72:73]
	v_pk_add_f32 v[6:7], v[6:7], v[70:71]
	s_waitcnt vmcnt(12)
	v_pk_add_f32 v[4:5], v[4:5], v[68:69]
	v_pk_add_f32 v[2:3], v[2:3], v[66:67]
	global_store_dwordx4 v[14:15], v[30:33], off
	global_store_dwordx4 v[14:15], v[10:13], off offset:64
	global_store_dwordx4 v[14:15], v[6:9], off offset:512
	global_store_dwordx4 v[14:15], v[2:5], off offset:576
	s_cbranch_vccnz .LBB0_652
	s_andn2_b64 vcc, exec, s[12:13]
	s_cbranch_vccnz .LBB0_651
	s_barrier
	s_branch .LBB0_651

.LBB0_786:
	v_pk_mul_f32 v[156:157], v[126:127], s[44:45] op_sel_hi:[1,0]
	v_pk_mul_f32 v[122:123], v[126:127], v[122:123]
	v_exp_f32_e32 v156, v156
	v_exp_f32_e32 v157, v157
	v_pk_mul_f32 v[126:127], v[118:119], s[44:45] op_sel_hi:[1,0]
	v_pk_mul_f32 v[158:159], v[128:129], s[44:45] op_sel_hi:[1,0]
	v_exp_f32_e32 v126, v126
	v_exp_f32_e32 v127, v127
	v_pk_fma_f32 v[156:157], v[156:157], s[50:51], s[50:51] op_sel_hi:[1,0,0]
	v_pk_mul_f32 v[124:125], v[128:129], v[124:125]
	v_pk_mul_f32 v[128:129], v[120:121], s[44:45] op_sel_hi:[1,0]
	v_exp_f32_e32 v158, v158
	v_exp_f32_e32 v159, v159
	v_rcp_f32_e32 v156, v156
	v_rcp_f32_e32 v157, v157
	v_exp_f32_e32 v128, v128
	v_exp_f32_e32 v129, v129
	v_pk_fma_f32 v[126:127], v[126:127], s[50:51], s[50:51] op_sel_hi:[1,0,0]
	v_pk_fma_f32 v[158:159], v[158:159], s[50:51], s[50:51] op_sel_hi:[1,0,0]
	v_rcp_f32_e32 v126, v126
	v_rcp_f32_e32 v127, v127
	v_pk_mul_f32 v[122:123], v[156:157], v[122:123]
	v_pk_fma_f32 v[128:129], v[128:129], s[50:51], s[50:51] op_sel_hi:[1,0,0]
	v_pk_mul_f32 v[114:115], v[118:119], v[114:115]
	v_rcp_f32_e32 v158, v158
	v_rcp_f32_e32 v159, v159
	v_rcp_f32_e32 v128, v128
	v_rcp_f32_e32 v129, v129
	v_pk_mul_f32 v[116:117], v[120:121], v[116:117]
	v_pk_mul_f32 v[114:115], v[126:127], v[114:115]
	v_med3_f32 v119, v122, s80, v154
	v_med3_f32 v120, v123, s80, v154
	v_cvt_pk_fp8_f32 v118, v119, v120
	v_med3_f32 v114, v114, s80, v154
	v_med3_f32 v115, v115, s80, v154
	v_cvt_pk_fp8_f32 v119, v114, v115
	v_pk_mul_f32 v[124:125], v[158:159], v[124:125]
	v_pk_mul_f32 v[116:117], v[128:129], v[116:117]
	v_med3_f32 v120, v124, s80, v154
	v_med3_f32 v121, v125, s80, v154
	v_med3_f32 v114, v116, s80, v154
	v_med3_f32 v115, v117, s80, v154
	v_cvt_pk_fp8_f32 v118, v120, v121 op_sel:[0,0,1]
	v_cvt_pk_fp8_f32 v119, v114, v115 op_sel:[0,0,1]
	v_lshl_add_u32 v155, s60, 8, v148
	v_lshl_or_b32 v144, s2, 7, v150
	v_mov_b64_e32 v[146:147], s[14:15]
	v_ashrrev_i32_e32 v145, 31, v144
	v_mad_i64_i32 v[114:115], s[26:27], v155, s75, v[146:147]
	v_lshl_add_u64 v[114:115], v[114:115], 0, v[144:145]
	global_store_dwordx2 v[114:115], v[118:119], off
	v_pk_mul_f32 v[114:115], v[110:111], s[44:45] op_sel_hi:[1,0]
	v_pk_mul_f32 v[106:107], v[110:111], v[106:107]
	v_exp_f32_e32 v114, v114
	v_exp_f32_e32 v115, v115
	v_pk_mul_f32 v[110:111], v[102:103], s[44:45] op_sel_hi:[1,0]
	v_pk_mul_f32 v[116:117], v[112:113], s[44:45] op_sel_hi:[1,0]
	v_exp_f32_e32 v110, v110
	v_exp_f32_e32 v111, v111
	v_pk_fma_f32 v[114:115], v[114:115], s[50:51], s[50:51] op_sel_hi:[1,0,0]
	v_pk_mul_f32 v[108:109], v[112:113], v[108:109]
	v_pk_mul_f32 v[112:113], v[104:105], s[44:45] op_sel_hi:[1,0]
	v_exp_f32_e32 v116, v116
	v_exp_f32_e32 v117, v117
	v_rcp_f32_e32 v114, v114
	v_rcp_f32_e32 v115, v115
	v_exp_f32_e32 v112, v112
	v_exp_f32_e32 v113, v113
	v_pk_fma_f32 v[110:111], v[110:111], s[50:51], s[50:51] op_sel_hi:[1,0,0]
	v_pk_fma_f32 v[116:117], v[116:117], s[50:51], s[50:51] op_sel_hi:[1,0,0]
	v_rcp_f32_e32 v110, v110
	v_rcp_f32_e32 v111, v111
	v_pk_mul_f32 v[106:107], v[114:115], v[106:107]
	v_pk_fma_f32 v[112:113], v[112:113], s[50:51], s[50:51] op_sel_hi:[1,0,0]
	v_pk_mul_f32 v[98:99], v[102:103], v[98:99]
	v_rcp_f32_e32 v116, v116
	v_rcp_f32_e32 v117, v117
	v_rcp_f32_e32 v112, v112
	v_rcp_f32_e32 v113, v113
	v_pk_mul_f32 v[100:101], v[104:105], v[100:101]
	v_pk_mul_f32 v[98:99], v[110:111], v[98:99]
	v_med3_f32 v103, v106, s80, v154
	v_med3_f32 v104, v107, s80, v154
	v_cvt_pk_fp8_f32 v102, v103, v104
	v_med3_f32 v98, v98, s80, v154
	v_med3_f32 v99, v99, s80, v154
	v_cvt_pk_fp8_f32 v103, v98, v99
	v_pk_mul_f32 v[108:109], v[116:117], v[108:109]
	v_pk_mul_f32 v[100:101], v[112:113], v[100:101]
	v_med3_f32 v104, v108, s80, v154
	v_med3_f32 v105, v109, s80, v154
	v_med3_f32 v98, v100, s80, v154
	v_med3_f32 v99, v101, s80, v154
	v_cvt_pk_fp8_f32 v102, v104, v105 op_sel:[0,0,1]
	v_cvt_pk_fp8_f32 v103, v98, v99 op_sel:[0,0,1]
	v_or_b32_e32 v118, 16, v155
	v_mad_i64_i32 v[98:99], s[26:27], v118, s75, v[146:147]
	v_lshl_add_u64 v[98:99], v[98:99], 0, v[144:145]
	global_store_dwordx2 v[98:99], v[102:103], off
	v_pk_mul_f32 v[98:99], v[94:95], s[44:45] op_sel_hi:[1,0]
	v_pk_mul_f32 v[90:91], v[94:95], v[90:91]
	v_exp_f32_e32 v98, v98
	v_exp_f32_e32 v99, v99
	v_pk_mul_f32 v[94:95], v[86:87], s[44:45] op_sel_hi:[1,0]
	v_pk_mul_f32 v[100:101], v[96:97], s[44:45] op_sel_hi:[1,0]
	v_exp_f32_e32 v94, v94
	v_exp_f32_e32 v95, v95
	v_pk_fma_f32 v[98:99], v[98:99], s[50:51], s[50:51] op_sel_hi:[1,0,0]
	v_pk_mul_f32 v[92:93], v[96:97], v[92:93]
	v_pk_mul_f32 v[96:97], v[88:89], s[44:45] op_sel_hi:[1,0]
	v_exp_f32_e32 v100, v100
	v_exp_f32_e32 v101, v101
	v_rcp_f32_e32 v98, v98
	v_rcp_f32_e32 v99, v99
	v_exp_f32_e32 v96, v96
	v_exp_f32_e32 v97, v97
	v_pk_fma_f32 v[94:95], v[94:95], s[50:51], s[50:51] op_sel_hi:[1,0,0]
	v_pk_fma_f32 v[100:101], v[100:101], s[50:51], s[50:51] op_sel_hi:[1,0,0]
	v_rcp_f32_e32 v94, v94
	v_rcp_f32_e32 v95, v95
	v_pk_mul_f32 v[90:91], v[98:99], v[90:91]
	v_pk_fma_f32 v[96:97], v[96:97], s[50:51], s[50:51] op_sel_hi:[1,0,0]
	v_pk_mul_f32 v[82:83], v[86:87], v[82:83]
	v_rcp_f32_e32 v100, v100
	v_rcp_f32_e32 v101, v101
	v_rcp_f32_e32 v96, v96
	v_rcp_f32_e32 v97, v97
	v_pk_mul_f32 v[84:85], v[88:89], v[84:85]
	v_pk_mul_f32 v[82:83], v[94:95], v[82:83]
	v_med3_f32 v87, v90, s80, v154
	v_med3_f32 v88, v91, s80, v154
	v_cvt_pk_fp8_f32 v86, v87, v88
	v_med3_f32 v82, v82, s80, v154
	v_med3_f32 v83, v83, s80, v154
	v_cvt_pk_fp8_f32 v87, v82, v83
	v_pk_mul_f32 v[92:93], v[100:101], v[92:93]
	v_pk_mul_f32 v[84:85], v[96:97], v[84:85]
	v_med3_f32 v88, v92, s80, v154
	v_med3_f32 v89, v93, s80, v154
	v_med3_f32 v82, v84, s80, v154
	v_med3_f32 v83, v85, s80, v154
	v_cvt_pk_fp8_f32 v86, v88, v89 op_sel:[0,0,1]
	v_cvt_pk_fp8_f32 v87, v82, v83 op_sel:[0,0,1]
	v_or_b32_e32 v102, 32, v155
	v_mad_i64_i32 v[82:83], s[26:27], v102, s75, v[146:147]
	v_lshl_add_u64 v[82:83], v[82:83], 0, v[144:145]
	global_store_dwordx2 v[82:83], v[86:87], off
	v_pk_mul_f32 v[82:83], v[78:79], s[44:45] op_sel_hi:[1,0]
	v_pk_mul_f32 v[74:75], v[78:79], v[74:75]
	v_exp_f32_e32 v82, v82
	v_exp_f32_e32 v83, v83
	v_pk_mul_f32 v[78:79], v[70:71], s[44:45] op_sel_hi:[1,0]
	v_pk_mul_f32 v[84:85], v[80:81], s[44:45] op_sel_hi:[1,0]
	v_exp_f32_e32 v78, v78
	v_exp_f32_e32 v79, v79
	v_pk_fma_f32 v[82:83], v[82:83], s[50:51], s[50:51] op_sel_hi:[1,0,0]
	v_pk_mul_f32 v[76:77], v[80:81], v[76:77]
	v_pk_mul_f32 v[80:81], v[72:73], s[44:45] op_sel_hi:[1,0]
	v_exp_f32_e32 v84, v84
	v_exp_f32_e32 v85, v85
	v_rcp_f32_e32 v82, v82
	v_rcp_f32_e32 v83, v83
	v_exp_f32_e32 v80, v80
	v_exp_f32_e32 v81, v81
	v_pk_fma_f32 v[78:79], v[78:79], s[50:51], s[50:51] op_sel_hi:[1,0,0]
	v_pk_fma_f32 v[84:85], v[84:85], s[50:51], s[50:51] op_sel_hi:[1,0,0]
	v_rcp_f32_e32 v78, v78
	v_rcp_f32_e32 v79, v79
	v_pk_mul_f32 v[74:75], v[82:83], v[74:75]
	v_pk_fma_f32 v[80:81], v[80:81], s[50:51], s[50:51] op_sel_hi:[1,0,0]
	v_pk_mul_f32 v[66:67], v[70:71], v[66:67]
	v_rcp_f32_e32 v84, v84
	v_rcp_f32_e32 v85, v85
	v_rcp_f32_e32 v80, v80
	v_rcp_f32_e32 v81, v81
	v_pk_mul_f32 v[68:69], v[72:73], v[68:69]
	v_pk_mul_f32 v[66:67], v[78:79], v[66:67]
	v_med3_f32 v71, v74, s80, v154
	v_med3_f32 v72, v75, s80, v154
	v_cvt_pk_fp8_f32 v70, v71, v72
	v_med3_f32 v66, v66, s80, v154
	v_med3_f32 v67, v67, s80, v154
	v_cvt_pk_fp8_f32 v71, v66, v67
	v_pk_mul_f32 v[76:77], v[84:85], v[76:77]
	v_pk_mul_f32 v[68:69], v[80:81], v[68:69]
	v_med3_f32 v72, v76, s80, v154
	v_med3_f32 v73, v77, s80, v154
	v_med3_f32 v66, v68, s80, v154
	v_med3_f32 v67, v69, s80, v154
	v_cvt_pk_fp8_f32 v70, v72, v73 op_sel:[0,0,1]
	v_cvt_pk_fp8_f32 v71, v66, v67 op_sel:[0,0,1]
	v_or_b32_e32 v86, 48, v155
	v_mad_i64_i32 v[66:67], s[26:27], v86, s75, v[146:147]
	v_lshl_add_u64 v[66:67], v[66:67], 0, v[144:145]
	global_store_dwordx2 v[66:67], v[70:71], off
	s_setprio 0
	v_pk_mul_f32 v[66:67], v[62:63], s[44:45] op_sel_hi:[1,0]
	v_pk_mul_f32 v[58:59], v[62:63], v[58:59]
	v_exp_f32_e32 v66, v66
	v_exp_f32_e32 v67, v67
	v_pk_mul_f32 v[62:63], v[54:55], s[44:45] op_sel_hi:[1,0]
	v_pk_mul_f32 v[68:69], v[64:65], s[44:45] op_sel_hi:[1,0]
	v_exp_f32_e32 v62, v62
	v_exp_f32_e32 v63, v63
	v_pk_fma_f32 v[66:67], v[66:67], s[50:51], s[50:51] op_sel_hi:[1,0,0]
	v_pk_mul_f32 v[60:61], v[64:65], v[60:61]
	v_pk_mul_f32 v[64:65], v[56:57], s[44:45] op_sel_hi:[1,0]
	v_exp_f32_e32 v68, v68
	v_exp_f32_e32 v69, v69
	v_rcp_f32_e32 v66, v66
	v_rcp_f32_e32 v67, v67
	v_exp_f32_e32 v64, v64
	v_exp_f32_e32 v65, v65
	v_pk_fma_f32 v[62:63], v[62:63], s[50:51], s[50:51] op_sel_hi:[1,0,0]
	v_pk_fma_f32 v[68:69], v[68:69], s[50:51], s[50:51] op_sel_hi:[1,0,0]
	v_rcp_f32_e32 v62, v62
	v_rcp_f32_e32 v63, v63
	v_pk_mul_f32 v[58:59], v[66:67], v[58:59]
	v_pk_fma_f32 v[64:65], v[64:65], s[50:51], s[50:51] op_sel_hi:[1,0,0]
	v_pk_mul_f32 v[50:51], v[54:55], v[50:51]
	v_rcp_f32_e32 v68, v68
	v_rcp_f32_e32 v69, v69
	v_rcp_f32_e32 v64, v64
	v_rcp_f32_e32 v65, v65
	v_pk_mul_f32 v[52:53], v[56:57], v[52:53]
	v_pk_mul_f32 v[50:51], v[62:63], v[50:51]
	v_med3_f32 v55, v58, s80, v154
	v_med3_f32 v56, v59, s80, v154
	v_cvt_pk_fp8_f32 v54, v55, v56
	v_med3_f32 v50, v50, s80, v154
	v_med3_f32 v51, v51, s80, v154
	v_cvt_pk_fp8_f32 v55, v50, v51
	v_pk_mul_f32 v[60:61], v[68:69], v[60:61]
	v_pk_mul_f32 v[52:53], v[64:65], v[52:53]
	v_med3_f32 v56, v60, s80, v154
	v_med3_f32 v57, v61, s80, v154
	v_med3_f32 v50, v52, s80, v154
	v_med3_f32 v51, v53, s80, v154
	v_cvt_pk_fp8_f32 v54, v56, v57 op_sel:[0,0,1]
	v_cvt_pk_fp8_f32 v55, v50, v51 op_sel:[0,0,1]
	v_add_u32_e32 v70, 0x80, v155
	v_mad_i64_i32 v[50:51], s[26:27], v70, s75, v[146:147]
	v_lshl_add_u64 v[50:51], v[50:51], 0, v[144:145]
	global_store_dwordx2 v[50:51], v[54:55], off
	v_pk_mul_f32 v[50:51], v[46:47], s[44:45] op_sel_hi:[1,0]
	v_pk_mul_f32 v[42:43], v[46:47], v[42:43]
	v_exp_f32_e32 v50, v50
	v_exp_f32_e32 v51, v51
	v_pk_mul_f32 v[46:47], v[38:39], s[44:45] op_sel_hi:[1,0]
	v_pk_mul_f32 v[52:53], v[48:49], s[44:45] op_sel_hi:[1,0]
	v_exp_f32_e32 v46, v46
	v_exp_f32_e32 v47, v47
	v_pk_fma_f32 v[50:51], v[50:51], s[50:51], s[50:51] op_sel_hi:[1,0,0]
	v_pk_mul_f32 v[44:45], v[48:49], v[44:45]
	v_pk_mul_f32 v[48:49], v[40:41], s[44:45] op_sel_hi:[1,0]
	v_exp_f32_e32 v52, v52
	v_exp_f32_e32 v53, v53
	v_rcp_f32_e32 v50, v50
	v_rcp_f32_e32 v51, v51
	v_exp_f32_e32 v48, v48
	v_exp_f32_e32 v49, v49
	v_pk_fma_f32 v[46:47], v[46:47], s[50:51], s[50:51] op_sel_hi:[1,0,0]
	v_pk_fma_f32 v[52:53], v[52:53], s[50:51], s[50:51] op_sel_hi:[1,0,0]
	v_rcp_f32_e32 v46, v46
	v_rcp_f32_e32 v47, v47
	v_pk_mul_f32 v[42:43], v[50:51], v[42:43]
	v_pk_fma_f32 v[48:49], v[48:49], s[50:51], s[50:51] op_sel_hi:[1,0,0]
	v_pk_mul_f32 v[34:35], v[38:39], v[34:35]
	v_rcp_f32_e32 v52, v52
	v_rcp_f32_e32 v53, v53
	v_rcp_f32_e32 v48, v48
	v_rcp_f32_e32 v49, v49
	v_pk_mul_f32 v[36:37], v[40:41], v[36:37]
	v_pk_mul_f32 v[34:35], v[46:47], v[34:35]
	v_med3_f32 v39, v42, s80, v154
	v_med3_f32 v40, v43, s80, v154
	v_cvt_pk_fp8_f32 v38, v39, v40
	v_med3_f32 v34, v34, s80, v154
	v_med3_f32 v35, v35, s80, v154
	v_cvt_pk_fp8_f32 v39, v34, v35
	v_pk_mul_f32 v[44:45], v[52:53], v[44:45]
	v_pk_mul_f32 v[36:37], v[48:49], v[36:37]
	v_med3_f32 v40, v44, s80, v154
	v_med3_f32 v41, v45, s80, v154
	v_med3_f32 v34, v36, s80, v154
	v_med3_f32 v35, v37, s80, v154
	v_cvt_pk_fp8_f32 v38, v40, v41 op_sel:[0,0,1]
	v_cvt_pk_fp8_f32 v39, v34, v35 op_sel:[0,0,1]
	v_add_u32_e32 v54, 0x90, v155
	v_mad_i64_i32 v[34:35], s[26:27], v54, s75, v[146:147]
	v_lshl_add_u64 v[34:35], v[34:35], 0, v[144:145]
	global_store_dwordx2 v[34:35], v[38:39], off
	v_pk_mul_f32 v[34:35], v[30:31], s[44:45] op_sel_hi:[1,0]
	v_pk_mul_f32 v[26:27], v[30:31], v[26:27]
	v_exp_f32_e32 v34, v34
	v_exp_f32_e32 v35, v35
	v_pk_mul_f32 v[30:31], v[22:23], s[44:45] op_sel_hi:[1,0]
	v_pk_mul_f32 v[36:37], v[32:33], s[44:45] op_sel_hi:[1,0]
	v_exp_f32_e32 v30, v30
	v_exp_f32_e32 v31, v31
	v_pk_fma_f32 v[34:35], v[34:35], s[50:51], s[50:51] op_sel_hi:[1,0,0]
	v_pk_mul_f32 v[28:29], v[32:33], v[28:29]
	v_pk_mul_f32 v[32:33], v[24:25], s[44:45] op_sel_hi:[1,0]
	v_exp_f32_e32 v36, v36
	v_exp_f32_e32 v37, v37
	v_rcp_f32_e32 v34, v34
	v_rcp_f32_e32 v35, v35
	v_exp_f32_e32 v32, v32
	v_exp_f32_e32 v33, v33
	v_pk_fma_f32 v[30:31], v[30:31], s[50:51], s[50:51] op_sel_hi:[1,0,0]
	v_pk_fma_f32 v[36:37], v[36:37], s[50:51], s[50:51] op_sel_hi:[1,0,0]
	v_rcp_f32_e32 v30, v30
	v_rcp_f32_e32 v31, v31
	v_pk_mul_f32 v[26:27], v[34:35], v[26:27]
	v_pk_fma_f32 v[32:33], v[32:33], s[50:51], s[50:51] op_sel_hi:[1,0,0]
	v_pk_mul_f32 v[18:19], v[22:23], v[18:19]
	v_rcp_f32_e32 v36, v36
	v_rcp_f32_e32 v37, v37
	v_rcp_f32_e32 v32, v32
	v_rcp_f32_e32 v33, v33
	v_pk_mul_f32 v[20:21], v[24:25], v[20:21]
	v_pk_mul_f32 v[18:19], v[30:31], v[18:19]
	v_med3_f32 v23, v26, s80, v154
	v_med3_f32 v24, v27, s80, v154
	v_cvt_pk_fp8_f32 v22, v23, v24
	v_med3_f32 v18, v18, s80, v154
	v_med3_f32 v19, v19, s80, v154
	v_cvt_pk_fp8_f32 v23, v18, v19
	v_pk_mul_f32 v[28:29], v[36:37], v[28:29]
	v_pk_mul_f32 v[20:21], v[32:33], v[20:21]
	v_med3_f32 v24, v28, s80, v154
	v_med3_f32 v25, v29, s80, v154
	v_med3_f32 v18, v20, s80, v154
	v_med3_f32 v19, v21, s80, v154
	v_cvt_pk_fp8_f32 v22, v24, v25 op_sel:[0,0,1]
	v_cvt_pk_fp8_f32 v23, v18, v19 op_sel:[0,0,1]
	v_add_u32_e32 v38, 0xa0, v155
	v_mad_i64_i32 v[18:19], s[26:27], v38, s75, v[146:147]
	v_lshl_add_u64 v[18:19], v[18:19], 0, v[144:145]
	global_store_dwordx2 v[18:19], v[22:23], off
	v_pk_mul_f32 v[18:19], v[14:15], s[44:45] op_sel_hi:[1,0]
	v_pk_mul_f32 v[10:11], v[14:15], v[10:11]
	v_exp_f32_e32 v18, v18
	v_exp_f32_e32 v19, v19
	v_pk_mul_f32 v[14:15], v[6:7], s[44:45] op_sel_hi:[1,0]
	v_pk_mul_f32 v[20:21], v[16:17], s[44:45] op_sel_hi:[1,0]
	v_exp_f32_e32 v14, v14
	v_exp_f32_e32 v15, v15
	v_pk_fma_f32 v[18:19], v[18:19], s[50:51], s[50:51] op_sel_hi:[1,0,0]
	v_pk_mul_f32 v[12:13], v[16:17], v[12:13]
	v_pk_mul_f32 v[16:17], v[8:9], s[44:45] op_sel_hi:[1,0]
	v_exp_f32_e32 v20, v20
	v_exp_f32_e32 v21, v21
	v_rcp_f32_e32 v18, v18
	v_rcp_f32_e32 v19, v19
	v_exp_f32_e32 v16, v16
	v_exp_f32_e32 v17, v17
	v_pk_fma_f32 v[14:15], v[14:15], s[50:51], s[50:51] op_sel_hi:[1,0,0]
	v_pk_fma_f32 v[20:21], v[20:21], s[50:51], s[50:51] op_sel_hi:[1,0,0]
	v_rcp_f32_e32 v14, v14
	v_rcp_f32_e32 v15, v15
	v_pk_mul_f32 v[10:11], v[18:19], v[10:11]
	v_pk_fma_f32 v[16:17], v[16:17], s[50:51], s[50:51] op_sel_hi:[1,0,0]
	v_pk_mul_f32 v[2:3], v[6:7], v[2:3]
	v_rcp_f32_e32 v20, v20
	v_rcp_f32_e32 v21, v21
	v_rcp_f32_e32 v16, v16
	v_rcp_f32_e32 v17, v17
	v_pk_mul_f32 v[4:5], v[8:9], v[4:5]
	v_pk_mul_f32 v[2:3], v[14:15], v[2:3]
	v_med3_f32 v7, v10, s80, v154
	v_med3_f32 v8, v11, s80, v154
	v_cvt_pk_fp8_f32 v6, v7, v8
	v_med3_f32 v2, v2, s80, v154
	v_med3_f32 v3, v3, s80, v154
	v_cvt_pk_fp8_f32 v7, v2, v3
	v_pk_mul_f32 v[12:13], v[20:21], v[12:13]
	v_pk_mul_f32 v[4:5], v[16:17], v[4:5]
	v_med3_f32 v8, v12, s80, v154
	v_med3_f32 v9, v13, s80, v154
	v_med3_f32 v2, v4, s80, v154
	v_med3_f32 v3, v5, s80, v154
	v_cvt_pk_fp8_f32 v6, v8, v9 op_sel:[0,0,1]
	v_cvt_pk_fp8_f32 v7, v2, v3 op_sel:[0,0,1]
	v_add_u32_e32 v22, 0xb0, v155
	v_mad_i64_i32 v[2:3], s[26:27], v22, s75, v[146:147]
	v_lshl_add_u64 v[2:3], v[2:3], 0, v[144:145]
	s_andn2_b64 vcc, exec, s[0:1]
	s_mov_b64 s[0:1], -1
	global_store_dwordx2 v[2:3], v[6:7], off
	s_cbranch_vccnz .LBB0_779
	s_andn2_b64 vcc, exec, s[12:13]
	s_cbranch_vccnz .LBB0_778
	s_barrier
	s_branch .LBB0_778

.LBB0_861:
	v_lshl_or_b32 v2, s71, 8, v184
	v_lshl_add_u32 v206, s2, 8, v182
	v_ashrrev_i32_e32 v3, 31, v2
	v_lshlrev_b64 v[176:177], 2, v[2:3]
	v_ashrrev_i32_e32 v207, 31, v206
	v_lshl_add_u64 v[178:179], s[78:79], 0, v[176:177]
	v_lshlrev_b64 v[180:181], 13, v[206:207]
	s_nop 15
	s_nop 15
	v_lshl_add_u64 v[14:15], v[178:179], 0, v[180:181]
	global_load_dwordx4 v[2:5], v[14:15], off
	global_load_dwordx4 v[6:9], v[14:15], off offset:64
	global_load_dwordx4 v[10:13], v[14:15], off offset:512
	s_nop 0
	global_load_dwordx4 v[14:17], v[14:15], off offset:576
	v_or_b32_e32 v18, 16, v206
	v_ashrrev_i32_e32 v19, 31, v18
	v_lshlrev_b64 v[224:225], 13, v[18:19]
	v_lshl_add_u64 v[30:31], v[178:179], 0, v[224:225]
	global_load_dwordx4 v[18:21], v[30:31], off
	global_load_dwordx4 v[22:25], v[30:31], off offset:64
	global_load_dwordx4 v[26:29], v[30:31], off offset:512
	s_nop 0
	global_load_dwordx4 v[30:33], v[30:31], off offset:576
	v_or_b32_e32 v190, 32, v206
	v_ashrrev_i32_e32 v191, 31, v190
	v_lshlrev_b64 v[226:227], 13, v[190:191]
	v_lshl_add_u64 v[202:203], v[178:179], 0, v[226:227]
	global_load_dwordx4 v[190:193], v[202:203], off
	global_load_dwordx4 v[194:197], v[202:203], off offset:64
	global_load_dwordx4 v[198:201], v[202:203], off offset:512
	s_nop 0
	global_load_dwordx4 v[202:205], v[202:203], off offset:576
	v_or_b32_e32 v206, 48, v206
	v_ashrrev_i32_e32 v207, 31, v206
	v_lshlrev_b64 v[228:229], 13, v[206:207]
	v_lshl_add_u64 v[220:221], v[178:179], 0, v[228:229]
	global_load_dwordx4 v[206:209], v[220:221], off
	global_load_dwordx4 v[210:213], v[220:221], off offset:64
	global_load_dwordx4 v[214:217], v[220:221], off offset:512
	s_nop 0
	global_load_dwordx4 v[220:223], v[220:221], off offset:576
	s_mov_b64 s[26:27], 0x100000
	s_mov_b64 s[50:51], -1
	s_and_b64 vcc, exec, s[0:1]
	s_waitcnt vmcnt(0)
	v_pk_add_f32 v[2:3], v[158:159], v[2:3]
	v_lshl_add_u64 v[158:159], s[78:79], 0, v[180:181]
	v_pk_add_f32 v[4:5], v[160:161], v[4:5]
	v_lshl_add_u64 v[158:159], v[158:159], 0, v[176:177]
	global_store_dwordx4 v[158:159], v[2:5], off
	s_nop 1
	v_pk_add_f32 v[4:5], v[156:157], v[8:9]
	v_pk_add_f32 v[2:3], v[154:155], v[6:7]
	global_store_dwordx4 v[158:159], v[2:5], off offset:64
	v_lshl_add_u64 v[6:7], s[78:79], 0, v[224:225]
	v_lshl_add_u64 v[6:7], v[6:7], 0, v[176:177]
	v_pk_add_f32 v[4:5], v[144:145], v[12:13]
	v_pk_add_f32 v[2:3], v[142:143], v[10:11]
	global_store_dwordx4 v[158:159], v[2:5], off offset:512
	s_nop 1
	v_pk_add_f32 v[4:5], v[136:137], v[16:17]
	v_pk_add_f32 v[2:3], v[134:135], v[14:15]
	global_store_dwordx4 v[158:159], v[2:5], off offset:576
	s_nop 1
	v_pk_add_f32 v[4:5], v[152:153], v[20:21]
	v_pk_add_f32 v[2:3], v[150:151], v[18:19]
	global_store_dwordx4 v[6:7], v[2:5], off
	s_nop 1
	v_pk_add_f32 v[4:5], v[148:149], v[24:25]
	v_pk_add_f32 v[2:3], v[146:147], v[22:23]
	global_store_dwordx4 v[6:7], v[2:5], off offset:64
	s_nop 1
	v_pk_add_f32 v[4:5], v[128:129], v[28:29]
	v_pk_add_f32 v[2:3], v[126:127], v[26:27]
	global_store_dwordx4 v[6:7], v[2:5], off offset:512
	s_nop 1
	v_pk_add_f32 v[4:5], v[120:121], v[32:33]
	v_pk_add_f32 v[2:3], v[118:119], v[30:31]
	global_store_dwordx4 v[6:7], v[2:5], off offset:576
	v_lshl_add_u64 v[6:7], s[78:79], 0, v[226:227]
	v_lshl_add_u64 v[6:7], v[6:7], 0, v[176:177]
	v_pk_add_f32 v[4:5], v[140:141], v[192:193]
	v_pk_add_f32 v[2:3], v[138:139], v[190:191]
	global_store_dwordx4 v[6:7], v[2:5], off
	s_nop 1
	v_pk_add_f32 v[4:5], v[132:133], v[196:197]
	v_pk_add_f32 v[2:3], v[130:131], v[194:195]
	global_store_dwordx4 v[6:7], v[2:5], off offset:64
	v_lshl_add_u64 v[130:131], v[180:181], 0, s[26:27]
	s_mov_b64 s[26:27], 0x120000
	v_pk_add_f32 v[4:5], v[112:113], v[200:201]
	v_pk_add_f32 v[2:3], v[110:111], v[198:199]
	global_store_dwordx4 v[6:7], v[2:5], off offset:512
	v_lshl_add_u64 v[136:137], v[180:181], 0, s[26:27]
	v_lshl_add_u64 v[18:19], v[178:179], 0, v[136:137]
	v_pk_add_f32 v[4:5], v[108:109], v[204:205]
	v_pk_add_f32 v[2:3], v[106:107], v[202:203]
	global_store_dwordx4 v[6:7], v[2:5], off offset:576
	v_lshl_add_u64 v[6:7], s[78:79], 0, v[228:229]
	v_lshl_add_u64 v[6:7], v[6:7], 0, v[176:177]
	v_pk_add_f32 v[4:5], v[124:125], v[208:209]
	v_pk_add_f32 v[2:3], v[122:123], v[206:207]
	global_store_dwordx4 v[6:7], v[2:5], off
	s_mov_b64 s[26:27], 0x140000
	v_lshl_add_u64 v[132:133], v[180:181], 0, s[26:27]
	v_pk_add_f32 v[4:5], v[116:117], v[212:213]
	v_pk_add_f32 v[2:3], v[114:115], v[210:211]
	global_store_dwordx4 v[6:7], v[2:5], off offset:64
	s_mov_b64 s[26:27], 0x160000
	v_lshl_add_u64 v[134:135], v[180:181], 0, s[26:27]
	v_pk_add_f32 v[4:5], v[104:105], v[216:217]
	v_pk_add_f32 v[2:3], v[102:103], v[214:215]
	global_store_dwordx4 v[6:7], v[2:5], off offset:512
	v_lshl_add_u64 v[122:123], v[178:179], 0, v[134:135]
	s_nop 0
	v_pk_add_f32 v[4:5], v[100:101], v[222:223]
	v_pk_add_f32 v[2:3], v[98:99], v[220:221]
	global_store_dwordx4 v[6:7], v[2:5], off offset:576
	s_setprio 0
	s_nop 1
	v_lshl_add_u64 v[2:3], v[178:179], 0, v[130:131]
	global_load_dwordx4 v[14:17], v[2:3], off
	global_load_dwordx4 v[10:13], v[2:3], off offset:64
	global_load_dwordx4 v[6:9], v[2:3], off offset:512
	s_nop 0
	global_load_dwordx4 v[2:5], v[2:3], off offset:576
	s_nop 0
	global_load_dwordx4 v[110:113], v[18:19], off
	global_load_dwordx4 v[106:109], v[18:19], off offset:64
	global_load_dwordx4 v[98:101], v[18:19], off offset:512
	global_load_dwordx4 v[26:29], v[18:19], off offset:576
	v_lshl_add_u64 v[18:19], v[178:179], 0, v[132:133]
	global_load_dwordx4 v[102:105], v[18:19], off
	global_load_dwordx4 v[30:33], v[18:19], off offset:64
	global_load_dwordx4 v[22:25], v[18:19], off offset:512
	s_nop 0
	global_load_dwordx4 v[18:21], v[18:19], off offset:576
	s_nop 0
	global_load_dwordx4 v[118:121], v[122:123], off
	global_load_dwordx4 v[114:117], v[122:123], off offset:64
	global_load_dwordx4 v[126:129], v[122:123], off offset:512
	s_nop 0
	global_load_dwordx4 v[122:125], v[122:123], off offset:576
	s_waitcnt vmcnt(15)
	v_pk_add_f32 v[14:15], v[94:95], v[14:15]
	v_lshl_add_u64 v[94:95], s[78:79], 0, v[130:131]
	v_lshl_add_u64 v[94:95], v[94:95], 0, v[176:177]
	s_waitcnt vmcnt(13)
	v_pk_add_f32 v[8:9], v[84:85], v[8:9]
	v_pk_add_f32 v[6:7], v[82:83], v[6:7]
	global_store_dwordx4 v[94:95], v[6:9], off offset:512
	s_waitcnt vmcnt(13)
	v_pk_add_f32 v[4:5], v[76:77], v[4:5]
	v_pk_add_f32 v[2:3], v[74:75], v[2:3]
	v_lshl_add_u64 v[6:7], s[78:79], 0, v[136:137]
	global_store_dwordx4 v[94:95], v[2:5], off offset:576
	v_lshl_add_u64 v[6:7], v[6:7], 0, v[176:177]
	v_pk_add_f32 v[16:17], v[96:97], v[16:17]
	s_waitcnt vmcnt(13)
	v_pk_add_f32 v[4:5], v[88:89], v[112:113]
	v_pk_add_f32 v[2:3], v[86:87], v[110:111]
	global_store_dwordx4 v[6:7], v[2:5], off
	v_pk_add_f32 v[12:13], v[92:93], v[12:13]
	v_pk_add_f32 v[10:11], v[90:91], v[10:11]
	s_waitcnt vmcnt(13)
	v_pk_add_f32 v[4:5], v[80:81], v[108:109]
	v_pk_add_f32 v[2:3], v[78:79], v[106:107]
	global_store_dwordx4 v[6:7], v[2:5], off offset:64
	global_store_dwordx4 v[94:95], v[14:17], off
	global_store_dwordx4 v[94:95], v[10:13], off offset:64
	s_waitcnt vmcnt(15)
	v_pk_add_f32 v[4:5], v[68:69], v[100:101]
	v_pk_add_f32 v[2:3], v[66:67], v[98:99]
	global_store_dwordx4 v[6:7], v[2:5], off offset:512
	s_waitcnt vmcnt(15)
	s_nop 0
	v_pk_add_f32 v[4:5], v[60:61], v[28:29]
	v_pk_add_f32 v[2:3], v[58:59], v[26:27]
	global_store_dwordx4 v[6:7], v[2:5], off offset:576
	v_lshl_add_u64 v[6:7], s[78:79], 0, v[132:133]
	v_lshl_add_u64 v[6:7], v[6:7], 0, v[176:177]
	s_waitcnt vmcnt(15)
	v_pk_add_f32 v[4:5], v[72:73], v[104:105]
	v_pk_add_f32 v[2:3], v[70:71], v[102:103]
	global_store_dwordx4 v[6:7], v[2:5], off
	s_waitcnt vmcnt(15)
	s_nop 0
	v_pk_add_f32 v[4:5], v[64:65], v[32:33]
	v_pk_add_f32 v[2:3], v[62:63], v[30:31]
	global_store_dwordx4 v[6:7], v[2:5], off offset:64
	s_waitcnt vmcnt(15)
	s_nop 0
	v_pk_add_f32 v[4:5], v[52:53], v[24:25]
	v_pk_add_f32 v[2:3], v[50:51], v[22:23]
	global_store_dwordx4 v[6:7], v[2:5], off offset:512
	s_waitcnt vmcnt(15)
	s_nop 0
	v_pk_add_f32 v[4:5], v[44:45], v[20:21]
	v_pk_add_f32 v[2:3], v[42:43], v[18:19]
	global_store_dwordx4 v[6:7], v[2:5], off offset:576
	v_lshl_add_u64 v[6:7], s[78:79], 0, v[134:135]
	v_lshl_add_u64 v[6:7], v[6:7], 0, v[176:177]
	s_waitcnt vmcnt(15)
	v_pk_add_f32 v[4:5], v[56:57], v[120:121]
	v_pk_add_f32 v[2:3], v[54:55], v[118:119]
	global_store_dwordx4 v[6:7], v[2:5], off
	s_waitcnt vmcnt(15)
	s_nop 0
	v_pk_add_f32 v[4:5], v[48:49], v[116:117]
	v_pk_add_f32 v[2:3], v[46:47], v[114:115]
	global_store_dwordx4 v[6:7], v[2:5], off offset:64
	s_waitcnt vmcnt(15)
	s_nop 0
	v_pk_add_f32 v[4:5], v[40:41], v[128:129]
	v_pk_add_f32 v[2:3], v[38:39], v[126:127]
	global_store_dwordx4 v[6:7], v[2:5], off offset:512
	s_waitcnt vmcnt(15)
	s_nop 0
	v_pk_add_f32 v[4:5], v[36:37], v[124:125]
	v_pk_add_f32 v[2:3], v[34:35], v[122:123]
	global_store_dwordx4 v[6:7], v[2:5], off offset:576
	s_cbranch_vccnz .LBB0_846
	s_andn2_b64 vcc, exec, s[14:15]
	s_cbranch_vccnz .LBB0_845
	s_barrier
	s_branch .LBB0_845

.LBB0_988:
	s_lshl_b32 s27, s2, 8
	s_add_i32 s41, s27, 0xfffff400
	s_cmp_gt_i32 s2, 11
	s_mov_b32 s45, 0x37400000
	s_movk_i32 s26, 0x400
	s_cselect_b32 s45, s45, 0x31400000
	s_cselect_b32 s26, s26, 0xc00
	s_cselect_b32 s27, s41, s27
	s_add_u32 s56, s28, s45
	s_addc_u32 s57, s29, 0
	v_or_b32_e32 v4, s27, v184
	s_cmp_lt_i32 s2, 4
	v_lshl_add_u32 v3, s54, 8, v182
	s_cselect_b64 vcc, -1, 0
	v_ashrrev_i32_e32 v5, 31, v4
	v_cndmask_b32_e32 v2, 1.0, v190, vcc
	v_lshl_add_u64 v[4:5], v[4:5], 1, s[56:57]
	v_mad_i64_i32 v[6:7], s[56:57], s26, v3, 0
	v_lshl_add_u64 v[10:11], v[6:7], 1, v[4:5]
	v_pk_mul_f32 v[6:7], v[2:3], v[158:159] op_sel_hi:[0,1]
	s_nop 15
	s_nop 15
	v_pk_mul_f32 v[8:9], v[2:3], v[160:161] op_sel_hi:[0,1]
	v_cvt_pk_bf16_f32 v6, v6, v7
	v_cvt_pk_bf16_f32 v7, v8, v9
	v_pk_mul_f32 v[12:13], v[2:3], v[156:157] op_sel_hi:[0,1]
	v_pk_mul_f32 v[14:15], v[2:3], v[154:155] op_sel_hi:[0,1]
	v_cvt_pk_bf16_f32 v8, v14, v15
	v_cvt_pk_bf16_f32 v9, v12, v13
	global_store_dwordx4 v[10:11], v[6:9], off
	v_pk_mul_f32 v[12:13], v[2:3], v[144:145] op_sel_hi:[0,1]
	v_pk_mul_f32 v[14:15], v[2:3], v[142:143] op_sel_hi:[0,1]
	v_pk_mul_f32 v[6:7], v[2:3], v[150:151] op_sel_hi:[0,1]
	v_pk_mul_f32 v[8:9], v[2:3], v[152:153] op_sel_hi:[0,1]
	v_cvt_pk_bf16_f32 v6, v6, v7
	v_cvt_pk_bf16_f32 v7, v8, v9
	v_cvt_pk_bf16_f32 v8, v14, v15
	v_cvt_pk_bf16_f32 v9, v12, v13
	global_store_dwordx4 v[10:11], v[6:9], off offset:256
	v_pk_mul_f32 v[12:13], v[2:3], v[140:141] op_sel_hi:[0,1]
	v_pk_mul_f32 v[14:15], v[2:3], v[138:139] op_sel_hi:[0,1]
	v_or_b32_e32 v6, 16, v3
	v_mad_i64_i32 v[6:7], s[56:57], s26, v6, 0
	v_lshl_add_u64 v[10:11], v[6:7], 1, v[4:5]
	v_pk_mul_f32 v[6:7], v[2:3], v[146:147] op_sel_hi:[0,1]
	v_pk_mul_f32 v[8:9], v[2:3], v[148:149] op_sel_hi:[0,1]
	v_cvt_pk_bf16_f32 v6, v6, v7
	v_cvt_pk_bf16_f32 v7, v8, v9
	v_cvt_pk_bf16_f32 v8, v14, v15
	v_cvt_pk_bf16_f32 v9, v12, v13
	global_store_dwordx4 v[10:11], v[6:9], off
	v_pk_mul_f32 v[12:13], v[2:3], v[128:129] op_sel_hi:[0,1]
	v_pk_mul_f32 v[14:15], v[2:3], v[126:127] op_sel_hi:[0,1]
	v_pk_mul_f32 v[6:7], v[2:3], v[134:135] op_sel_hi:[0,1]
	v_pk_mul_f32 v[8:9], v[2:3], v[136:137] op_sel_hi:[0,1]
	v_cvt_pk_bf16_f32 v6, v6, v7
	v_cvt_pk_bf16_f32 v7, v8, v9
	v_cvt_pk_bf16_f32 v8, v14, v15
	v_cvt_pk_bf16_f32 v9, v12, v13
	global_store_dwordx4 v[10:11], v[6:9], off offset:256
	v_pk_mul_f32 v[12:13], v[2:3], v[124:125] op_sel_hi:[0,1]
	v_pk_mul_f32 v[14:15], v[2:3], v[122:123] op_sel_hi:[0,1]
	v_or_b32_e32 v6, 32, v3
	v_mad_i64_i32 v[6:7], s[56:57], s26, v6, 0
	v_lshl_add_u64 v[10:11], v[6:7], 1, v[4:5]
	v_pk_mul_f32 v[6:7], v[2:3], v[130:131] op_sel_hi:[0,1]
	v_pk_mul_f32 v[8:9], v[2:3], v[132:133] op_sel_hi:[0,1]
	v_cvt_pk_bf16_f32 v6, v6, v7
	v_cvt_pk_bf16_f32 v7, v8, v9
	v_cvt_pk_bf16_f32 v8, v14, v15
	v_cvt_pk_bf16_f32 v9, v12, v13
	global_store_dwordx4 v[10:11], v[6:9], off
	v_pk_mul_f32 v[12:13], v[2:3], v[112:113] op_sel_hi:[0,1]
	v_pk_mul_f32 v[14:15], v[2:3], v[110:111] op_sel_hi:[0,1]
	v_pk_mul_f32 v[6:7], v[2:3], v[118:119] op_sel_hi:[0,1]
	v_pk_mul_f32 v[8:9], v[2:3], v[120:121] op_sel_hi:[0,1]
	v_cvt_pk_bf16_f32 v6, v6, v7
	v_cvt_pk_bf16_f32 v7, v8, v9
	v_cvt_pk_bf16_f32 v8, v14, v15
	v_cvt_pk_bf16_f32 v9, v12, v13
	global_store_dwordx4 v[10:11], v[6:9], off offset:256
	v_pk_mul_f32 v[12:13], v[2:3], v[108:109] op_sel_hi:[0,1]
	v_pk_mul_f32 v[14:15], v[2:3], v[106:107] op_sel_hi:[0,1]
	v_or_b32_e32 v6, 48, v3
	v_mad_i64_i32 v[6:7], s[56:57], s26, v6, 0
	v_lshl_add_u64 v[10:11], v[6:7], 1, v[4:5]
	v_pk_mul_f32 v[6:7], v[2:3], v[114:115] op_sel_hi:[0,1]
	v_pk_mul_f32 v[8:9], v[2:3], v[116:117] op_sel_hi:[0,1]
	v_cvt_pk_bf16_f32 v6, v6, v7
	v_cvt_pk_bf16_f32 v7, v8, v9
	v_cvt_pk_bf16_f32 v8, v14, v15
	v_cvt_pk_bf16_f32 v9, v12, v13
	global_store_dwordx4 v[10:11], v[6:9], off
	v_pk_mul_f32 v[12:13], v[2:3], v[100:101] op_sel_hi:[0,1]
	v_pk_mul_f32 v[14:15], v[2:3], v[98:99] op_sel_hi:[0,1]
	v_pk_mul_f32 v[6:7], v[2:3], v[102:103] op_sel_hi:[0,1]
	v_pk_mul_f32 v[8:9], v[2:3], v[104:105] op_sel_hi:[0,1]
	v_cvt_pk_bf16_f32 v6, v6, v7
	v_cvt_pk_bf16_f32 v7, v8, v9
	v_cvt_pk_bf16_f32 v8, v14, v15
	v_cvt_pk_bf16_f32 v9, v12, v13
	global_store_dwordx4 v[10:11], v[6:9], off offset:256
	s_setprio 0
	v_pk_mul_f32 v[12:13], v[2:3], v[92:93] op_sel_hi:[0,1]
	v_pk_mul_f32 v[14:15], v[2:3], v[90:91] op_sel_hi:[0,1]
	v_add_u32_e32 v6, 0x80, v3
	v_mad_i64_i32 v[6:7], s[56:57], s26, v6, 0
	v_lshl_add_u64 v[10:11], v[6:7], 1, v[4:5]
	v_pk_mul_f32 v[6:7], v[2:3], v[94:95] op_sel_hi:[0,1]
	v_pk_mul_f32 v[8:9], v[2:3], v[96:97] op_sel_hi:[0,1]
	v_cvt_pk_bf16_f32 v6, v6, v7
	v_cvt_pk_bf16_f32 v7, v8, v9
	v_cvt_pk_bf16_f32 v8, v14, v15
	v_cvt_pk_bf16_f32 v9, v12, v13
	global_store_dwordx4 v[10:11], v[6:9], off
	v_pk_mul_f32 v[12:13], v[2:3], v[80:81] op_sel_hi:[0,1]
	v_pk_mul_f32 v[14:15], v[2:3], v[78:79] op_sel_hi:[0,1]
	v_pk_mul_f32 v[6:7], v[2:3], v[86:87] op_sel_hi:[0,1]
	v_pk_mul_f32 v[8:9], v[2:3], v[88:89] op_sel_hi:[0,1]
	v_cvt_pk_bf16_f32 v6, v6, v7
	v_cvt_pk_bf16_f32 v7, v8, v9
	v_cvt_pk_bf16_f32 v8, v14, v15
	v_cvt_pk_bf16_f32 v9, v12, v13
	global_store_dwordx4 v[10:11], v[6:9], off offset:256
	v_pk_mul_f32 v[12:13], v[2:3], v[76:77] op_sel_hi:[0,1]
	v_pk_mul_f32 v[14:15], v[2:3], v[74:75] op_sel_hi:[0,1]
	v_add_u32_e32 v6, 0x90, v3
	v_mad_i64_i32 v[6:7], s[56:57], s26, v6, 0
	v_lshl_add_u64 v[10:11], v[6:7], 1, v[4:5]
	v_pk_mul_f32 v[6:7], v[2:3], v[82:83] op_sel_hi:[0,1]
	v_pk_mul_f32 v[8:9], v[2:3], v[84:85] op_sel_hi:[0,1]
	v_cvt_pk_bf16_f32 v6, v6, v7
	v_cvt_pk_bf16_f32 v7, v8, v9
	v_cvt_pk_bf16_f32 v8, v14, v15
	v_cvt_pk_bf16_f32 v9, v12, v13
	global_store_dwordx4 v[10:11], v[6:9], off
	v_pk_mul_f32 v[12:13], v[2:3], v[64:65] op_sel_hi:[0,1]
	v_pk_mul_f32 v[14:15], v[2:3], v[62:63] op_sel_hi:[0,1]
	v_pk_mul_f32 v[6:7], v[2:3], v[70:71] op_sel_hi:[0,1]
	v_pk_mul_f32 v[8:9], v[2:3], v[72:73] op_sel_hi:[0,1]
	v_cvt_pk_bf16_f32 v6, v6, v7
	v_cvt_pk_bf16_f32 v7, v8, v9
	v_cvt_pk_bf16_f32 v8, v14, v15
	v_cvt_pk_bf16_f32 v9, v12, v13
	global_store_dwordx4 v[10:11], v[6:9], off offset:256
	v_pk_mul_f32 v[12:13], v[2:3], v[60:61] op_sel_hi:[0,1]
	v_pk_mul_f32 v[14:15], v[2:3], v[58:59] op_sel_hi:[0,1]
	v_add_u32_e32 v6, 0xa0, v3
	v_mad_i64_i32 v[6:7], s[56:57], s26, v6, 0
	v_lshl_add_u64 v[10:11], v[6:7], 1, v[4:5]
	v_pk_mul_f32 v[6:7], v[2:3], v[66:67] op_sel_hi:[0,1]
	v_pk_mul_f32 v[8:9], v[2:3], v[68:69] op_sel_hi:[0,1]
	v_cvt_pk_bf16_f32 v6, v6, v7
	v_cvt_pk_bf16_f32 v7, v8, v9
	v_cvt_pk_bf16_f32 v8, v14, v15
	v_cvt_pk_bf16_f32 v9, v12, v13
	global_store_dwordx4 v[10:11], v[6:9], off
	v_pk_mul_f32 v[12:13], v[2:3], v[48:49] op_sel_hi:[0,1]
	v_pk_mul_f32 v[14:15], v[2:3], v[46:47] op_sel_hi:[0,1]
	v_pk_mul_f32 v[6:7], v[2:3], v[54:55] op_sel_hi:[0,1]
	v_pk_mul_f32 v[8:9], v[2:3], v[56:57] op_sel_hi:[0,1]
	v_cvt_pk_bf16_f32 v6, v6, v7
	v_cvt_pk_bf16_f32 v7, v8, v9
	v_add_u32_e32 v3, 0xb0, v3
	v_cvt_pk_bf16_f32 v8, v14, v15
	v_cvt_pk_bf16_f32 v9, v12, v13
	global_store_dwordx4 v[10:11], v[6:9], off offset:256
	v_pk_mul_f32 v[10:11], v[2:3], v[44:45] op_sel_hi:[0,1]
	v_pk_mul_f32 v[12:13], v[2:3], v[42:43] op_sel_hi:[0,1]
	v_mad_i64_i32 v[6:7], s[26:27], s26, v3, 0
	v_lshl_add_u64 v[8:9], v[6:7], 1, v[4:5]
	v_pk_mul_f32 v[4:5], v[2:3], v[50:51] op_sel_hi:[0,1]
	v_pk_mul_f32 v[6:7], v[2:3], v[52:53] op_sel_hi:[0,1]
	v_cvt_pk_bf16_f32 v4, v4, v5
	v_cvt_pk_bf16_f32 v5, v6, v7
	v_cvt_pk_bf16_f32 v6, v12, v13
	v_cvt_pk_bf16_f32 v7, v10, v11
	global_store_dwordx4 v[8:9], v[4:7], off
	s_andn2_b64 vcc, exec, s[0:1]
	s_mov_b64 s[0:1], -1
	v_pk_mul_f32 v[4:5], v[2:3], v[40:41] op_sel_hi:[0,1]
	v_pk_mul_f32 v[6:7], v[2:3], v[38:39] op_sel_hi:[0,1]
	v_pk_mul_f32 v[10:11], v[2:3], v[36:37] op_sel_hi:[0,1]
	v_pk_mul_f32 v[12:13], v[2:3], v[34:35] op_sel_hi:[0,1]
	v_cvt_pk_bf16_f32 v2, v6, v7
	v_cvt_pk_bf16_f32 v3, v4, v5
	v_cvt_pk_bf16_f32 v4, v12, v13
	v_cvt_pk_bf16_f32 v5, v10, v11
	global_store_dwordx4 v[8:9], v[2:5], off offset:256
	s_cbranch_vccnz .LBB0_977
	s_andn2_b64 vcc, exec, s[12:13]
	s_cbranch_vccnz .LBB0_976
	s_barrier
	s_branch .LBB0_976

.LBB0_1195:
	v_lshl_or_b32 v146, s2, 8, v198
	v_ashrrev_i32_e32 v147, 31, v146
	v_lshl_add_u64 v[66:67], v[146:147], 2, s[42:43]
	global_load_dwordx4 v[86:89], v[66:67], off
	global_load_dwordx4 v[82:85], v[66:67], off offset:16
	global_load_dwordx4 v[70:73], v[66:67], off offset:512
	s_nop 0
	global_load_dwordx4 v[66:69], v[66:67], off offset:528
	v_lshl_add_u32 v186, s54, 8, v196
	v_ashrrev_i32_e32 v187, 31, v186
	v_lshlrev_b64 v[184:185], 1, v[146:147]
	v_lshlrev_b64 v[146:147], 11, v[186:187]
	v_lshl_add_u64 v[188:189], s[4:5], 0, v[184:185]
	v_lshl_add_u64 v[146:147], v[188:189], 0, v[146:147]
	global_load_dwordx4 v[202:205], v[146:147], off
	global_load_dwordx4 v[166:169], v[146:147], off offset:256
	v_or_b32_e32 v194, 16, v186
	v_or_b32_e32 v192, 32, v186
	v_or_b32_e32 v190, 48, v186
	v_ashrrev_i32_e32 v195, 31, v194
	v_ashrrev_i32_e32 v193, 31, v192
	v_readlane_b32 s26, v254, 58
	v_ashrrev_i32_e32 v191, 31, v190
	v_lshlrev_b64 v[146:147], 12, v[186:187]
	v_lshlrev_b64 v[148:149], 11, v[194:195]
	v_lshlrev_b64 v[150:151], 11, v[192:193]
	v_readlane_b32 s27, v254, 59
	v_lshlrev_b64 v[152:153], 11, v[190:191]
	v_lshl_add_u64 v[148:149], v[188:189], 0, v[148:149]
	v_lshl_add_u64 v[146:147], s[26:27], 0, v[146:147]
	v_lshl_add_u64 v[150:151], v[188:189], 0, v[150:151]
	v_lshl_add_u64 v[210:211], v[188:189], 0, v[152:153]
	v_lshl_add_u64 v[212:213], v[146:147], 0, v[184:185]
	global_load_dwordx4 v[206:209], v[148:149], off
	global_load_dwordx4 v[162:165], v[148:149], off offset:256
	global_load_dwordx4 v[158:161], v[150:151], off
	global_load_dwordx4 v[154:157], v[150:151], off offset:256
	s_nop 0
	global_load_dwordx4 v[150:153], v[210:211], off
	global_load_dwordx4 v[146:149], v[210:211], off offset:256
	s_andn2_b64 vcc, exec, s[0:1]
	s_mov_b64 s[0:1], -1
	s_waitcnt vmcnt(0)
	v_pk_add_f32 v[142:143], v[142:143], v[86:87]
	v_pk_add_f32 v[144:145], v[144:145], v[88:89]
	v_pk_add_f32 v[140:141], v[140:141], v[84:85]
	v_pk_add_f32 v[214:215], v[130:131], v[66:67]
	v_pk_mul_f32 v[130:131], v[142:143], s[38:39] op_sel_hi:[1,0]
	v_pk_add_f32 v[138:139], v[138:139], v[82:83]
	v_pk_add_f32 v[210:211], v[132:133], v[68:69]
	v_pk_mul_f32 v[132:133], v[144:145], s[38:39] op_sel_hi:[1,0]
	v_exp_f32_e32 v130, v130
	v_exp_f32_e32 v131, v131
	v_pk_mul_f32 v[138:139], v[138:139], s[38:39] op_sel_hi:[1,0]
	v_pk_mul_f32 v[140:141], v[140:141], s[38:39] op_sel_hi:[1,0]
	v_exp_f32_e32 v132, v132
	v_exp_f32_e32 v133, v133
	v_exp_f32_e32 v138, v138
	v_exp_f32_e32 v139, v139
	v_exp_f32_e32 v140, v140
	v_exp_f32_e32 v141, v141
	v_pk_add_f32 v[136:137], v[136:137], v[72:73]
	v_pk_add_f32 v[130:131], v[130:131], 1.0 op_sel_hi:[1,0]
	v_pk_mul_f32 v[136:137], v[136:137], s[38:39] op_sel_hi:[1,0]
	v_pk_add_f32 v[132:133], v[132:133], 1.0 op_sel_hi:[1,0]
	v_rcp_f32_e32 v130, v130
	v_rcp_f32_e32 v131, v131
	v_exp_f32_e32 v136, v136
	v_exp_f32_e32 v137, v137
	v_pk_add_f32 v[138:139], v[138:139], 1.0 op_sel_hi:[1,0]
	v_pk_add_f32 v[140:141], v[140:141], 1.0 op_sel_hi:[1,0]
	v_rcp_f32_e32 v132, v132
	v_rcp_f32_e32 v133, v133
	v_rcp_f32_e32 v138, v138
	v_rcp_f32_e32 v139, v139
	v_rcp_f32_e32 v140, v140
	v_rcp_f32_e32 v141, v141
	v_lshlrev_b32_e32 v142, 16, v202
	v_and_b32_e32 v143, 0xffff0000, v202
	v_lshlrev_b32_e32 v144, 16, v203
	v_and_b32_e32 v145, 0xffff0000, v203
	v_pk_mul_f32 v[130:131], v[142:143], v[130:131]
	v_pk_add_f32 v[134:135], v[134:135], v[70:71]
	v_lshlrev_b32_e32 v202, 16, v204
	v_and_b32_e32 v203, 0xffff0000, v204
	v_lshlrev_b32_e32 v204, 16, v205
	v_and_b32_e32 v205, 0xffff0000, v205
	v_pk_add_f32 v[136:137], v[136:137], 1.0 op_sel_hi:[1,0]
	v_pk_mul_f32 v[132:133], v[144:145], v[132:133]
	v_cvt_pk_bf16_f32 v130, v130, v131
	v_pk_mul_f32 v[134:135], v[134:135], s[38:39] op_sel_hi:[1,0]
	v_cvt_pk_bf16_f32 v131, v132, v133
	v_pk_mul_f32 v[138:139], v[202:203], v[138:139]
	v_pk_mul_f32 v[140:141], v[204:205], v[140:141]
	v_cvt_pk_bf16_f32 v132, v138, v139
	v_exp_f32_e32 v134, v134
	v_cvt_pk_bf16_f32 v133, v140, v141
	global_store_dwordx4 v[212:213], v[130:133], off offset:2048
	v_exp_f32_e32 v135, v135
	v_pk_mul_f32 v[138:139], v[210:211], s[38:39] op_sel_hi:[1,0]
	v_rcp_f32_e32 v130, v136
	v_rcp_f32_e32 v131, v137
	v_pk_mul_f32 v[136:137], v[214:215], s[38:39] op_sel_hi:[1,0]
	v_pk_add_f32 v[126:127], v[126:127], v[86:87]
	v_exp_f32_e32 v136, v136
	v_exp_f32_e32 v137, v137
	v_exp_f32_e32 v138, v138
	v_exp_f32_e32 v139, v139
	v_pk_add_f32 v[122:123], v[122:123], v[82:83]
	v_pk_mul_f32 v[126:127], v[126:127], s[38:39] op_sel_hi:[1,0]
	v_pk_mul_f32 v[122:123], v[122:123], s[38:39] op_sel_hi:[1,0]
	v_exp_f32_e32 v126, v126
	v_exp_f32_e32 v127, v127
	v_pk_add_f32 v[128:129], v[128:129], v[88:89]
	v_exp_f32_e32 v122, v122
	v_exp_f32_e32 v123, v123
	v_pk_add_f32 v[134:135], v[134:135], 1.0 op_sel_hi:[1,0]
	v_pk_add_f32 v[136:137], v[136:137], 1.0 op_sel_hi:[1,0]
	v_pk_add_f32 v[124:125], v[124:125], v[84:85]
	v_pk_mul_f32 v[128:129], v[128:129], s[38:39] op_sel_hi:[1,0]
	v_rcp_f32_e32 v134, v134
	v_rcp_f32_e32 v135, v135
	v_rcp_f32_e32 v136, v136
	v_rcp_f32_e32 v137, v137
	v_pk_add_f32 v[138:139], v[138:139], 1.0 op_sel_hi:[1,0]
	v_exp_f32_e32 v128, v128
	v_exp_f32_e32 v129, v129
	v_pk_mul_f32 v[124:125], v[124:125], s[38:39] op_sel_hi:[1,0]
	v_pk_add_f32 v[118:119], v[118:119], v[70:71]
	v_rcp_f32_e32 v138, v138
	v_rcp_f32_e32 v139, v139
	v_pk_add_f32 v[126:127], v[126:127], 1.0 op_sel_hi:[1,0]
	v_exp_f32_e32 v124, v124
	v_exp_f32_e32 v125, v125
	v_pk_add_f32 v[120:121], v[120:121], v[72:73]
	v_pk_add_f32 v[114:115], v[114:115], v[66:67]
	v_pk_mul_f32 v[118:119], v[118:119], s[38:39] op_sel_hi:[1,0]
	v_lshlrev_b32_e32 v132, 16, v167
	v_and_b32_e32 v133, 0xffff0000, v167
	v_rcp_f32_e32 v126, v126
	v_rcp_f32_e32 v127, v127
	v_pk_add_f32 v[122:123], v[122:123], 1.0 op_sel_hi:[1,0]
	v_pk_add_f32 v[116:117], v[116:117], v[68:69]
	v_exp_f32_e32 v118, v118
	v_exp_f32_e32 v119, v119
	v_pk_mul_f32 v[120:121], v[120:121], s[38:39] op_sel_hi:[1,0]
	v_pk_mul_f32 v[114:115], v[114:115], s[38:39] op_sel_hi:[1,0]
	v_lshlrev_b32_e32 v216, 16, v166
	v_and_b32_e32 v217, 0xffff0000, v166
	v_pk_mul_f32 v[132:133], v[132:133], v[130:131]
	v_lshlrev_b32_e32 v130, 16, v168
	v_and_b32_e32 v131, 0xffff0000, v168
	v_rcp_f32_e32 v122, v122
	v_rcp_f32_e32 v123, v123
	v_exp_f32_e32 v120, v120
	v_exp_f32_e32 v121, v121
	v_exp_f32_e32 v114, v114
	v_exp_f32_e32 v115, v115
	v_pk_mul_f32 v[116:117], v[116:117], s[38:39] op_sel_hi:[1,0]
	v_pk_add_f32 v[110:111], v[110:111], v[86:87]
	v_pk_mul_f32 v[134:135], v[216:217], v[134:135]
	v_lshlrev_b32_e32 v140, 16, v169
	v_and_b32_e32 v141, 0xffff0000, v169
	v_pk_mul_f32 v[136:137], v[130:131], v[136:137]
	v_cvt_pk_bf16_f32 v130, v134, v135
	v_cvt_pk_bf16_f32 v131, v132, v133
	v_pk_add_f32 v[128:129], v[128:129], 1.0 op_sel_hi:[1,0]
	v_exp_f32_e32 v116, v116
	v_exp_f32_e32 v117, v117
	v_pk_add_f32 v[106:107], v[106:107], v[82:83]
	v_pk_mul_f32 v[110:111], v[110:111], s[38:39] op_sel_hi:[1,0]
	v_pk_mul_f32 v[138:139], v[140:141], v[138:139]
	v_cvt_pk_bf16_f32 v132, v136, v137
	v_rcp_f32_e32 v128, v128
	v_cvt_pk_bf16_f32 v133, v138, v139
	global_store_dwordx4 v[212:213], v[130:133], off offset:2304
	v_rcp_f32_e32 v129, v129
	v_pk_add_f32 v[124:125], v[124:125], 1.0 op_sel_hi:[1,0]
	v_lshlrev_b32_e32 v130, 16, v206
	v_and_b32_e32 v131, 0xffff0000, v206
	v_exp_f32_e32 v110, v110
	v_exp_f32_e32 v111, v111
	v_pk_mul_f32 v[106:107], v[106:107], s[38:39] op_sel_hi:[1,0]
	v_pk_mul_f32 v[126:127], v[126:127], v[130:131]
	v_lshlrev_b32_e32 v130, 16, v208
	v_and_b32_e32 v131, 0xffff0000, v208
	v_rcp_f32_e32 v124, v124
	v_rcp_f32_e32 v125, v125
	v_pk_add_f32 v[118:119], v[118:119], 1.0 op_sel_hi:[1,0]
	v_pk_add_f32 v[112:113], v[112:113], v[88:89]
	v_exp_f32_e32 v106, v106
	v_exp_f32_e32 v107, v107
	v_pk_mul_f32 v[130:131], v[122:123], v[130:131]
	v_cvt_pk_bf16_f32 v122, v126, v127
	v_lshlrev_b64 v[126:127], 12, v[194:195]
	v_rcp_f32_e32 v118, v118
	v_rcp_f32_e32 v119, v119
	v_pk_add_f32 v[120:121], v[120:121], 1.0 op_sel_hi:[1,0]
	v_pk_add_f32 v[114:115], v[114:115], 1.0 op_sel_hi:[1,0]
	v_pk_add_f32 v[108:109], v[108:109], v[84:85]
	v_pk_mul_f32 v[112:113], v[112:113], s[38:39] op_sel_hi:[1,0]
	v_lshlrev_b32_e32 v132, 16, v207
	v_and_b32_e32 v133, 0xffff0000, v207
	v_lshl_add_u64 v[126:127], s[26:27], 0, v[126:127]
	v_rcp_f32_e32 v120, v120
	v_rcp_f32_e32 v121, v121
	v_rcp_f32_e32 v114, v114
	v_rcp_f32_e32 v115, v115
	v_pk_add_f32 v[116:117], v[116:117], 1.0 op_sel_hi:[1,0]
	v_exp_f32_e32 v112, v112
	v_exp_f32_e32 v113, v113
	v_pk_mul_f32 v[108:109], v[108:109], s[38:39] op_sel_hi:[1,0]
	v_pk_add_f32 v[102:103], v[102:103], v[70:71]
	v_pk_mul_f32 v[128:129], v[128:129], v[132:133]
	v_lshlrev_b32_e32 v132, 16, v209
	v_and_b32_e32 v133, 0xffff0000, v209
	v_cvt_pk_bf16_f32 v123, v128, v129
	v_lshl_add_u64 v[126:127], v[126:127], 0, v[184:185]
	v_rcp_f32_e32 v116, v116
	v_rcp_f32_e32 v117, v117
	v_pk_add_f32 v[110:111], v[110:111], 1.0 op_sel_hi:[1,0]
	v_exp_f32_e32 v108, v108
	v_exp_f32_e32 v109, v109
	v_pk_add_f32 v[104:105], v[104:105], v[72:73]
	v_pk_add_f32 v[98:99], v[98:99], v[66:67]
	v_pk_mul_f32 v[102:103], v[102:103], s[38:39] op_sel_hi:[1,0]
	v_pk_mul_f32 v[132:133], v[124:125], v[132:133]
	v_cvt_pk_bf16_f32 v124, v130, v131
	v_rcp_f32_e32 v110, v110
	v_cvt_pk_bf16_f32 v125, v132, v133
	global_store_dwordx4 v[126:127], v[122:125], off offset:2048
	v_rcp_f32_e32 v111, v111
	v_pk_add_f32 v[106:107], v[106:107], 1.0 op_sel_hi:[1,0]
	v_lshlrev_b32_e32 v122, 16, v162
	v_and_b32_e32 v123, 0xffff0000, v162
	v_pk_add_f32 v[100:101], v[100:101], v[68:69]
	v_exp_f32_e32 v102, v102
	v_exp_f32_e32 v103, v103
	v_pk_mul_f32 v[104:105], v[104:105], s[38:39] op_sel_hi:[1,0]
	v_pk_mul_f32 v[98:99], v[98:99], s[38:39] op_sel_hi:[1,0]
	v_lshlrev_b32_e32 v124, 16, v163
	v_and_b32_e32 v125, 0xffff0000, v163
	v_pk_mul_f32 v[118:119], v[118:119], v[122:123]
	v_lshlrev_b32_e32 v122, 16, v164
	v_and_b32_e32 v123, 0xffff0000, v164
	v_rcp_f32_e32 v106, v106
	v_rcp_f32_e32 v107, v107
	v_exp_f32_e32 v104, v104
	v_exp_f32_e32 v105, v105
	v_exp_f32_e32 v98, v98
	v_exp_f32_e32 v99, v99
	v_pk_mul_f32 v[100:101], v[100:101], s[38:39] op_sel_hi:[1,0]
	v_pk_add_f32 v[94:95], v[94:95], v[86:87]
	v_pk_mul_f32 v[120:121], v[120:121], v[124:125]
	v_lshlrev_b32_e32 v124, 16, v165
	v_and_b32_e32 v125, 0xffff0000, v165
	v_pk_mul_f32 v[122:123], v[122:123], v[114:115]
	v_cvt_pk_bf16_f32 v114, v118, v119
	v_cvt_pk_bf16_f32 v115, v120, v121
	v_pk_add_f32 v[112:113], v[112:113], 1.0 op_sel_hi:[1,0]
	v_exp_f32_e32 v100, v100
	v_exp_f32_e32 v101, v101
	v_pk_add_f32 v[90:91], v[90:91], v[82:83]
	v_pk_mul_f32 v[94:95], v[94:95], s[38:39] op_sel_hi:[1,0]
	v_pk_mul_f32 v[124:125], v[124:125], v[116:117]
	v_cvt_pk_bf16_f32 v116, v122, v123
	v_rcp_f32_e32 v112, v112
	v_cvt_pk_bf16_f32 v117, v124, v125
	global_store_dwordx4 v[126:127], v[114:117], off offset:2304
	v_rcp_f32_e32 v113, v113
	v_pk_add_f32 v[108:109], v[108:109], 1.0 op_sel_hi:[1,0]
	v_lshlrev_b32_e32 v114, 16, v158
	v_and_b32_e32 v115, 0xffff0000, v158
	v_exp_f32_e32 v94, v94
	v_exp_f32_e32 v95, v95
	v_pk_mul_f32 v[90:91], v[90:91], s[38:39] op_sel_hi:[1,0]
	v_pk_mul_f32 v[110:111], v[110:111], v[114:115]
	v_lshlrev_b32_e32 v114, 16, v160
	v_and_b32_e32 v115, 0xffff0000, v160
	v_rcp_f32_e32 v108, v108
	v_rcp_f32_e32 v109, v109
	v_pk_add_f32 v[102:103], v[102:103], 1.0 op_sel_hi:[1,0]
	v_pk_add_f32 v[96:97], v[96:97], v[88:89]
	v_exp_f32_e32 v90, v90
	v_exp_f32_e32 v91, v91
	v_pk_mul_f32 v[114:115], v[106:107], v[114:115]
	v_cvt_pk_bf16_f32 v106, v110, v111
	v_lshlrev_b64 v[110:111], 12, v[192:193]
	v_rcp_f32_e32 v102, v102
	v_rcp_f32_e32 v103, v103
	v_pk_add_f32 v[104:105], v[104:105], 1.0 op_sel_hi:[1,0]
	v_pk_add_f32 v[98:99], v[98:99], 1.0 op_sel_hi:[1,0]
	v_pk_add_f32 v[92:93], v[92:93], v[84:85]
	v_pk_mul_f32 v[96:97], v[96:97], s[38:39] op_sel_hi:[1,0]
	v_lshlrev_b32_e32 v116, 16, v159
	v_and_b32_e32 v117, 0xffff0000, v159
	v_lshl_add_u64 v[110:111], s[26:27], 0, v[110:111]
	v_rcp_f32_e32 v104, v104
	v_rcp_f32_e32 v105, v105
	v_rcp_f32_e32 v98, v98
	v_rcp_f32_e32 v99, v99
	v_pk_add_f32 v[100:101], v[100:101], 1.0 op_sel_hi:[1,0]
	v_exp_f32_e32 v96, v96
	v_exp_f32_e32 v97, v97
	v_pk_mul_f32 v[92:93], v[92:93], s[38:39] op_sel_hi:[1,0]
	v_pk_add_f32 v[78:79], v[78:79], v[70:71]
	v_pk_mul_f32 v[112:113], v[112:113], v[116:117]
	v_lshlrev_b32_e32 v116, 16, v161
	v_and_b32_e32 v117, 0xffff0000, v161
	v_cvt_pk_bf16_f32 v107, v112, v113
	v_lshl_add_u64 v[110:111], v[110:111], 0, v[184:185]
	v_rcp_f32_e32 v100, v100
	v_rcp_f32_e32 v101, v101
	v_pk_add_f32 v[94:95], v[94:95], 1.0 op_sel_hi:[1,0]
	v_exp_f32_e32 v92, v92
	v_exp_f32_e32 v93, v93
	v_pk_add_f32 v[74:75], v[74:75], v[66:67]
	v_pk_mul_f32 v[78:79], v[78:79], s[38:39] op_sel_hi:[1,0]
	v_pk_mul_f32 v[116:117], v[108:109], v[116:117]
	v_cvt_pk_bf16_f32 v108, v114, v115
	v_rcp_f32_e32 v94, v94
	v_cvt_pk_bf16_f32 v109, v116, v117
	global_store_dwordx4 v[110:111], v[106:109], off offset:2048
	v_rcp_f32_e32 v95, v95
	v_pk_add_f32 v[90:91], v[90:91], 1.0 op_sel_hi:[1,0]
	v_lshlrev_b32_e32 v106, 16, v154
	v_and_b32_e32 v107, 0xffff0000, v154
	v_pk_add_f32 v[80:81], v[80:81], v[72:73]
	v_exp_f32_e32 v78, v78
	v_exp_f32_e32 v79, v79
	v_pk_mul_f32 v[74:75], v[74:75], s[38:39] op_sel_hi:[1,0]
	v_lshlrev_b32_e32 v108, 16, v155
	v_and_b32_e32 v109, 0xffff0000, v155
	v_pk_mul_f32 v[102:103], v[102:103], v[106:107]
	v_lshlrev_b32_e32 v106, 16, v156
	v_and_b32_e32 v107, 0xffff0000, v156
	v_rcp_f32_e32 v90, v90
	v_rcp_f32_e32 v91, v91
	v_pk_add_f32 v[76:77], v[76:77], v[68:69]
	v_pk_mul_f32 v[80:81], v[80:81], s[38:39] op_sel_hi:[1,0]
	v_exp_f32_e32 v74, v74
	v_exp_f32_e32 v75, v75
	v_pk_mul_f32 v[104:105], v[104:105], v[108:109]
	v_lshlrev_b32_e32 v108, 16, v157
	v_and_b32_e32 v109, 0xffff0000, v157
	v_pk_mul_f32 v[106:107], v[98:99], v[106:107]
	v_cvt_pk_bf16_f32 v98, v102, v103
	v_cvt_pk_bf16_f32 v99, v104, v105
	v_pk_add_f32 v[96:97], v[96:97], 1.0 op_sel_hi:[1,0]
	v_exp_f32_e32 v80, v80
	v_exp_f32_e32 v81, v81
	v_pk_mul_f32 v[76:77], v[76:77], s[38:39] op_sel_hi:[1,0]
	v_pk_mul_f32 v[108:109], v[100:101], v[108:109]
	v_cvt_pk_bf16_f32 v100, v106, v107
	v_rcp_f32_e32 v96, v96
	v_cvt_pk_bf16_f32 v101, v108, v109
	global_store_dwordx4 v[110:111], v[98:101], off offset:2304
	v_rcp_f32_e32 v97, v97
	v_pk_add_f32 v[92:93], v[92:93], 1.0 op_sel_hi:[1,0]
	v_lshlrev_b32_e32 v98, 16, v150
	v_and_b32_e32 v99, 0xffff0000, v150
	v_exp_f32_e32 v76, v76
	v_exp_f32_e32 v77, v77
	v_pk_mul_f32 v[94:95], v[94:95], v[98:99]
	v_lshlrev_b32_e32 v98, 16, v152
	v_and_b32_e32 v99, 0xffff0000, v152
	v_rcp_f32_e32 v92, v92
	v_rcp_f32_e32 v93, v93
	v_pk_add_f32 v[78:79], v[78:79], 1.0 op_sel_hi:[1,0]
	v_pk_mul_f32 v[98:99], v[90:91], v[98:99]
	v_cvt_pk_bf16_f32 v90, v94, v95
	v_lshlrev_b64 v[94:95], 12, v[190:191]
	v_rcp_f32_e32 v78, v78
	v_rcp_f32_e32 v79, v79
	v_pk_add_f32 v[74:75], v[74:75], 1.0 op_sel_hi:[1,0]
	v_lshlrev_b32_e32 v100, 16, v151
	v_and_b32_e32 v101, 0xffff0000, v151
	v_lshl_add_u64 v[94:95], s[26:27], 0, v[94:95]
	v_pk_add_f32 v[80:81], v[80:81], 1.0 op_sel_hi:[1,0]
	v_rcp_f32_e32 v74, v74
	v_rcp_f32_e32 v75, v75
	v_pk_mul_f32 v[96:97], v[96:97], v[100:101]
	v_lshlrev_b32_e32 v100, 16, v153
	v_and_b32_e32 v101, 0xffff0000, v153
	v_cvt_pk_bf16_f32 v91, v96, v97
	v_lshl_add_u64 v[94:95], v[94:95], 0, v[184:185]
	v_rcp_f32_e32 v80, v80
	v_rcp_f32_e32 v81, v81
	v_pk_add_f32 v[76:77], v[76:77], 1.0 op_sel_hi:[1,0]
	v_pk_mul_f32 v[100:101], v[92:93], v[100:101]
	v_cvt_pk_bf16_f32 v92, v98, v99
	v_rcp_f32_e32 v76, v76
	v_cvt_pk_bf16_f32 v93, v100, v101
	global_store_dwordx4 v[94:95], v[90:93], off offset:2048
	v_rcp_f32_e32 v77, v77
	v_add_u32_e32 v120, 0x80, v186
	v_lshlrev_b32_e32 v90, 16, v146
	v_and_b32_e32 v91, 0xffff0000, v146
	v_pk_mul_f32 v[78:79], v[78:79], v[90:91]
	v_lshlrev_b32_e32 v90, 16, v148
	v_and_b32_e32 v91, 0xffff0000, v148
	v_ashrrev_i32_e32 v121, 31, v120
	v_lshlrev_b32_e32 v92, 16, v147
	v_and_b32_e32 v93, 0xffff0000, v147
	v_pk_mul_f32 v[90:91], v[74:75], v[90:91]
	v_cvt_pk_bf16_f32 v74, v78, v79
	v_lshlrev_b64 v[78:79], 11, v[120:121]
	v_pk_mul_f32 v[80:81], v[80:81], v[92:93]
	v_lshlrev_b32_e32 v92, 16, v149
	v_and_b32_e32 v93, 0xffff0000, v149
	v_lshl_add_u64 v[78:79], v[188:189], 0, v[78:79]
	v_pk_mul_f32 v[92:93], v[76:77], v[92:93]
	v_cvt_pk_bf16_f32 v75, v80, v81
	v_cvt_pk_bf16_f32 v76, v90, v91
	v_add_u32_e32 v110, 0x90, v186
	v_cvt_pk_bf16_f32 v77, v92, v93
	global_load_dwordx4 v[112:115], v[78:79], off
	v_ashrrev_i32_e32 v111, 31, v110
	global_store_dwordx4 v[94:95], v[74:77], off offset:2304
	s_setprio 0
	global_load_dwordx4 v[116:119], v[78:79], off offset:256
	v_add_u32_e32 v108, 0xa0, v186
	v_lshlrev_b64 v[74:75], 11, v[110:111]
	v_lshl_add_u64 v[74:75], v[188:189], 0, v[74:75]
	global_load_dwordx4 v[102:105], v[74:75], off
	global_load_dwordx4 v[98:101], v[74:75], off offset:256
	v_ashrrev_i32_e32 v109, 31, v108
	v_lshlrev_b64 v[74:75], 11, v[108:109]
	v_lshl_add_u64 v[74:75], v[188:189], 0, v[74:75]
	global_load_dwordx4 v[94:97], v[74:75], off
	global_load_dwordx4 v[90:93], v[74:75], off offset:256
	v_add_u32_e32 v106, 0xb0, v186
	v_ashrrev_i32_e32 v107, 31, v106
	v_lshlrev_b64 v[74:75], 11, v[106:107]
	v_lshl_add_u64 v[74:75], v[188:189], 0, v[74:75]
	global_load_dwordx4 v[78:81], v[74:75], off
	s_nop 0
	global_load_dwordx4 v[74:77], v[74:75], off offset:256
	v_pk_add_f32 v[64:65], v[64:65], v[88:89]
	v_pk_add_f32 v[62:63], v[62:63], v[86:87]
	v_pk_add_f32 v[58:59], v[58:59], v[82:83]
	v_pk_mul_f32 v[62:63], v[62:63], s[38:39] op_sel_hi:[1,0]
	v_pk_mul_f32 v[64:65], v[64:65], s[38:39] op_sel_hi:[1,0]
	v_exp_f32_e32 v62, v62
	v_exp_f32_e32 v63, v63
	v_exp_f32_e32 v64, v64
	v_exp_f32_e32 v65, v65
	v_pk_mul_f32 v[58:59], v[58:59], s[38:39] op_sel_hi:[1,0]
	v_pk_add_f32 v[60:61], v[60:61], v[84:85]
	v_exp_f32_e32 v58, v58
	v_exp_f32_e32 v59, v59
	v_pk_mul_f32 v[60:61], v[60:61], s[38:39] op_sel_hi:[1,0]
	v_pk_add_f32 v[54:55], v[54:55], v[70:71]
	v_pk_add_f32 v[62:63], v[62:63], 1.0 op_sel_hi:[1,0]
	v_pk_add_f32 v[64:65], v[64:65], 1.0 op_sel_hi:[1,0]
	v_exp_f32_e32 v60, v60
	v_exp_f32_e32 v61, v61
	v_pk_add_f32 v[56:57], v[56:57], v[72:73]
	v_pk_add_f32 v[50:51], v[50:51], v[66:67]
	v_pk_mul_f32 v[54:55], v[54:55], s[38:39] op_sel_hi:[1,0]
	v_rcp_f32_e32 v62, v62
	v_rcp_f32_e32 v63, v63
	v_rcp_f32_e32 v64, v64
	v_rcp_f32_e32 v65, v65
	v_pk_add_f32 v[58:59], v[58:59], 1.0 op_sel_hi:[1,0]
	v_pk_add_f32 v[52:53], v[52:53], v[68:69]
	v_exp_f32_e32 v54, v54
	v_exp_f32_e32 v55, v55
	v_pk_mul_f32 v[56:57], v[56:57], s[38:39] op_sel_hi:[1,0]
	v_pk_mul_f32 v[50:51], v[50:51], s[38:39] op_sel_hi:[1,0]
	v_rcp_f32_e32 v58, v58
	v_rcp_f32_e32 v59, v59
	v_exp_f32_e32 v56, v56
	v_exp_f32_e32 v57, v57
	v_exp_f32_e32 v50, v50
	v_exp_f32_e32 v51, v51
	v_pk_mul_f32 v[52:53], v[52:53], s[38:39] op_sel_hi:[1,0]
	v_pk_add_f32 v[46:47], v[46:47], v[86:87]
	v_exp_f32_e32 v52, v52
	v_exp_f32_e32 v53, v53
	v_pk_add_f32 v[42:43], v[42:43], v[82:83]
	v_pk_mul_f32 v[46:47], v[46:47], s[38:39] op_sel_hi:[1,0]
	v_pk_add_f32 v[60:61], v[60:61], 1.0 op_sel_hi:[1,0]
	v_exp_f32_e32 v46, v46
	v_exp_f32_e32 v47, v47
	v_pk_mul_f32 v[42:43], v[42:43], s[38:39] op_sel_hi:[1,0]
	v_rcp_f32_e32 v60, v60
	v_rcp_f32_e32 v61, v61
	v_pk_add_f32 v[54:55], v[54:55], 1.0 op_sel_hi:[1,0]
	v_pk_add_f32 v[48:49], v[48:49], v[88:89]
	v_exp_f32_e32 v42, v42
	v_exp_f32_e32 v43, v43
	v_rcp_f32_e32 v54, v54
	v_rcp_f32_e32 v55, v55
	v_pk_add_f32 v[56:57], v[56:57], 1.0 op_sel_hi:[1,0]
	v_pk_add_f32 v[50:51], v[50:51], 1.0 op_sel_hi:[1,0]
	v_pk_add_f32 v[44:45], v[44:45], v[84:85]
	v_pk_mul_f32 v[48:49], v[48:49], s[38:39] op_sel_hi:[1,0]
	v_rcp_f32_e32 v56, v56
	v_rcp_f32_e32 v57, v57
	v_rcp_f32_e32 v50, v50
	s_waitcnt vmcnt(8)
	v_lshlrev_b32_e32 v122, 16, v112
	v_and_b32_e32 v123, 0xffff0000, v112
	v_lshlrev_b32_e32 v112, 16, v113
	v_and_b32_e32 v113, 0xffff0000, v113
	v_pk_mul_f32 v[62:63], v[62:63], v[122:123]
	v_pk_mul_f32 v[64:65], v[64:65], v[112:113]
	v_lshlrev_b32_e32 v112, 16, v114
	v_and_b32_e32 v113, 0xffff0000, v114
	v_pk_mul_f32 v[112:113], v[58:59], v[112:113]
	v_cvt_pk_bf16_f32 v58, v62, v63
	v_lshlrev_b64 v[62:63], 12, v[120:121]
	v_lshl_add_u64 v[62:63], s[26:27], 0, v[62:63]
	v_rcp_f32_e32 v51, v51
	v_pk_add_f32 v[52:53], v[52:53], 1.0 op_sel_hi:[1,0]
	v_exp_f32_e32 v48, v48
	v_exp_f32_e32 v49, v49
	v_pk_mul_f32 v[44:45], v[44:45], s[38:39] op_sel_hi:[1,0]
	v_pk_add_f32 v[38:39], v[38:39], v[70:71]
	v_lshlrev_b32_e32 v114, 16, v115
	v_and_b32_e32 v115, 0xffff0000, v115
	v_cvt_pk_bf16_f32 v59, v64, v65
	v_lshl_add_u64 v[62:63], v[62:63], 0, v[184:185]
	v_rcp_f32_e32 v52, v52
	v_rcp_f32_e32 v53, v53
	v_pk_add_f32 v[46:47], v[46:47], 1.0 op_sel_hi:[1,0]
	v_exp_f32_e32 v44, v44
	v_exp_f32_e32 v45, v45
	v_pk_add_f32 v[40:41], v[40:41], v[72:73]
	v_pk_add_f32 v[34:35], v[34:35], v[66:67]
	v_pk_mul_f32 v[38:39], v[38:39], s[38:39] op_sel_hi:[1,0]
	v_pk_mul_f32 v[114:115], v[60:61], v[114:115]
	v_cvt_pk_bf16_f32 v60, v112, v113
	v_rcp_f32_e32 v46, v46
	v_cvt_pk_bf16_f32 v61, v114, v115
	global_store_dwordx4 v[62:63], v[58:61], off offset:2048
	v_rcp_f32_e32 v47, v47
	v_pk_add_f32 v[42:43], v[42:43], 1.0 op_sel_hi:[1,0]
	s_waitcnt vmcnt(7)
	v_lshlrev_b32_e32 v58, 16, v116
	v_and_b32_e32 v59, 0xffff0000, v116
	v_pk_add_f32 v[36:37], v[36:37], v[68:69]
	v_exp_f32_e32 v38, v38
	v_exp_f32_e32 v39, v39
	v_pk_mul_f32 v[40:41], v[40:41], s[38:39] op_sel_hi:[1,0]
	v_pk_mul_f32 v[34:35], v[34:35], s[38:39] op_sel_hi:[1,0]
	v_lshlrev_b32_e32 v60, 16, v117
	v_and_b32_e32 v61, 0xffff0000, v117
	v_pk_mul_f32 v[54:55], v[54:55], v[58:59]
	v_lshlrev_b32_e32 v58, 16, v118
	v_and_b32_e32 v59, 0xffff0000, v118
	v_rcp_f32_e32 v42, v42
	v_rcp_f32_e32 v43, v43
	v_exp_f32_e32 v40, v40
	v_exp_f32_e32 v41, v41
	v_exp_f32_e32 v34, v34
	v_exp_f32_e32 v35, v35
	v_pk_mul_f32 v[36:37], v[36:37], s[38:39] op_sel_hi:[1,0]
	v_pk_add_f32 v[30:31], v[30:31], v[86:87]
	v_pk_mul_f32 v[56:57], v[56:57], v[60:61]
	v_lshlrev_b32_e32 v60, 16, v119
	v_and_b32_e32 v61, 0xffff0000, v119
	v_pk_mul_f32 v[58:59], v[50:51], v[58:59]
	v_cvt_pk_bf16_f32 v50, v54, v55
	v_cvt_pk_bf16_f32 v51, v56, v57
	v_pk_add_f32 v[48:49], v[48:49], 1.0 op_sel_hi:[1,0]
	v_exp_f32_e32 v36, v36
	v_exp_f32_e32 v37, v37
	v_pk_add_f32 v[26:27], v[26:27], v[82:83]
	v_pk_mul_f32 v[30:31], v[30:31], s[38:39] op_sel_hi:[1,0]
	v_pk_mul_f32 v[60:61], v[52:53], v[60:61]
	v_cvt_pk_bf16_f32 v52, v58, v59
	v_rcp_f32_e32 v48, v48
	v_cvt_pk_bf16_f32 v53, v60, v61
	global_store_dwordx4 v[62:63], v[50:53], off offset:2304
	v_rcp_f32_e32 v49, v49
	v_pk_add_f32 v[44:45], v[44:45], 1.0 op_sel_hi:[1,0]
	s_waitcnt vmcnt(7)
	v_lshlrev_b32_e32 v50, 16, v102
	v_and_b32_e32 v51, 0xffff0000, v102
	v_exp_f32_e32 v30, v30
	v_exp_f32_e32 v31, v31
	v_pk_mul_f32 v[26:27], v[26:27], s[38:39] op_sel_hi:[1,0]
	v_pk_mul_f32 v[46:47], v[46:47], v[50:51]
	v_lshlrev_b32_e32 v50, 16, v104
	v_and_b32_e32 v51, 0xffff0000, v104
	v_rcp_f32_e32 v44, v44
	v_rcp_f32_e32 v45, v45
	v_pk_add_f32 v[38:39], v[38:39], 1.0 op_sel_hi:[1,0]
	v_pk_add_f32 v[32:33], v[32:33], v[88:89]
	v_exp_f32_e32 v26, v26
	v_exp_f32_e32 v27, v27
	v_pk_mul_f32 v[50:51], v[42:43], v[50:51]
	v_cvt_pk_bf16_f32 v42, v46, v47
	v_lshlrev_b64 v[46:47], 12, v[110:111]
	v_rcp_f32_e32 v38, v38
	v_rcp_f32_e32 v39, v39
	v_pk_add_f32 v[40:41], v[40:41], 1.0 op_sel_hi:[1,0]
	v_pk_add_f32 v[34:35], v[34:35], 1.0 op_sel_hi:[1,0]
	v_pk_add_f32 v[28:29], v[28:29], v[84:85]
	v_pk_mul_f32 v[32:33], v[32:33], s[38:39] op_sel_hi:[1,0]
	v_lshlrev_b32_e32 v52, 16, v103
	v_and_b32_e32 v53, 0xffff0000, v103
	v_lshl_add_u64 v[46:47], s[26:27], 0, v[46:47]
	v_rcp_f32_e32 v40, v40
	v_rcp_f32_e32 v41, v41
	v_rcp_f32_e32 v34, v34
	v_rcp_f32_e32 v35, v35
	v_pk_add_f32 v[36:37], v[36:37], 1.0 op_sel_hi:[1,0]
	v_exp_f32_e32 v32, v32
	v_exp_f32_e32 v33, v33
	v_pk_mul_f32 v[28:29], v[28:29], s[38:39] op_sel_hi:[1,0]
	v_pk_add_f32 v[22:23], v[22:23], v[70:71]
	v_pk_mul_f32 v[48:49], v[48:49], v[52:53]
	v_lshlrev_b32_e32 v52, 16, v105
	v_and_b32_e32 v53, 0xffff0000, v105
	v_cvt_pk_bf16_f32 v43, v48, v49
	v_lshl_add_u64 v[46:47], v[46:47], 0, v[184:185]
	v_rcp_f32_e32 v36, v36
	v_rcp_f32_e32 v37, v37
	v_pk_add_f32 v[30:31], v[30:31], 1.0 op_sel_hi:[1,0]
	v_exp_f32_e32 v28, v28
	v_exp_f32_e32 v29, v29
	v_pk_add_f32 v[24:25], v[24:25], v[72:73]
	v_pk_add_f32 v[18:19], v[18:19], v[66:67]
	v_pk_mul_f32 v[22:23], v[22:23], s[38:39] op_sel_hi:[1,0]
	v_pk_mul_f32 v[52:53], v[44:45], v[52:53]
	v_cvt_pk_bf16_f32 v44, v50, v51
	v_rcp_f32_e32 v30, v30
	v_cvt_pk_bf16_f32 v45, v52, v53
	global_store_dwordx4 v[46:47], v[42:45], off offset:2048
	v_rcp_f32_e32 v31, v31
	v_pk_add_f32 v[26:27], v[26:27], 1.0 op_sel_hi:[1,0]
	s_waitcnt vmcnt(7)
	v_lshlrev_b32_e32 v42, 16, v98
	v_and_b32_e32 v43, 0xffff0000, v98
	v_pk_add_f32 v[20:21], v[20:21], v[68:69]
	v_exp_f32_e32 v22, v22
	v_exp_f32_e32 v23, v23
	v_pk_mul_f32 v[24:25], v[24:25], s[38:39] op_sel_hi:[1,0]
	v_pk_mul_f32 v[18:19], v[18:19], s[38:39] op_sel_hi:[1,0]
	v_lshlrev_b32_e32 v44, 16, v99
	v_and_b32_e32 v45, 0xffff0000, v99
	v_pk_mul_f32 v[38:39], v[38:39], v[42:43]
	v_lshlrev_b32_e32 v42, 16, v100
	v_and_b32_e32 v43, 0xffff0000, v100
	v_rcp_f32_e32 v26, v26
	v_rcp_f32_e32 v27, v27
	v_exp_f32_e32 v24, v24
	v_exp_f32_e32 v25, v25
	v_exp_f32_e32 v18, v18
	v_exp_f32_e32 v19, v19
	v_pk_mul_f32 v[20:21], v[20:21], s[38:39] op_sel_hi:[1,0]
	v_pk_add_f32 v[14:15], v[14:15], v[86:87]
	v_pk_mul_f32 v[40:41], v[40:41], v[44:45]
	v_lshlrev_b32_e32 v44, 16, v101
	v_and_b32_e32 v45, 0xffff0000, v101
	v_pk_mul_f32 v[42:43], v[34:35], v[42:43]
	v_cvt_pk_bf16_f32 v34, v38, v39
	v_cvt_pk_bf16_f32 v35, v40, v41
	v_pk_add_f32 v[32:33], v[32:33], 1.0 op_sel_hi:[1,0]
	v_exp_f32_e32 v20, v20
	v_exp_f32_e32 v21, v21
	v_pk_add_f32 v[10:11], v[10:11], v[82:83]
	v_pk_mul_f32 v[14:15], v[14:15], s[38:39] op_sel_hi:[1,0]
	v_pk_mul_f32 v[44:45], v[36:37], v[44:45]
	v_cvt_pk_bf16_f32 v36, v42, v43
	v_rcp_f32_e32 v32, v32
	v_cvt_pk_bf16_f32 v37, v44, v45
	global_store_dwordx4 v[46:47], v[34:37], off offset:2304
	v_rcp_f32_e32 v33, v33
	v_pk_add_f32 v[28:29], v[28:29], 1.0 op_sel_hi:[1,0]
	s_waitcnt vmcnt(7)
	v_lshlrev_b32_e32 v34, 16, v94
	v_and_b32_e32 v35, 0xffff0000, v94
	v_pk_add_f32 v[16:17], v[16:17], v[88:89]
	v_exp_f32_e32 v14, v14
	v_exp_f32_e32 v15, v15
	v_pk_mul_f32 v[10:11], v[10:11], s[38:39] op_sel_hi:[1,0]
	v_pk_mul_f32 v[30:31], v[30:31], v[34:35]
	v_lshlrev_b32_e32 v34, 16, v96
	v_and_b32_e32 v35, 0xffff0000, v96
	v_rcp_f32_e32 v28, v28
	v_rcp_f32_e32 v29, v29
	v_pk_add_f32 v[22:23], v[22:23], 1.0 op_sel_hi:[1,0]
	v_pk_add_f32 v[12:13], v[12:13], v[84:85]
	v_pk_mul_f32 v[16:17], v[16:17], s[38:39] op_sel_hi:[1,0]
	v_exp_f32_e32 v10, v10
	v_exp_f32_e32 v11, v11
	v_pk_mul_f32 v[34:35], v[26:27], v[34:35]
	v_cvt_pk_bf16_f32 v26, v30, v31
	v_lshlrev_b64 v[30:31], 12, v[108:109]
	v_rcp_f32_e32 v22, v22
	v_rcp_f32_e32 v23, v23
	v_pk_add_f32 v[24:25], v[24:25], 1.0 op_sel_hi:[1,0]
	v_pk_add_f32 v[18:19], v[18:19], 1.0 op_sel_hi:[1,0]
	v_exp_f32_e32 v16, v16
	v_exp_f32_e32 v17, v17
	v_pk_mul_f32 v[12:13], v[12:13], s[38:39] op_sel_hi:[1,0]
	v_lshlrev_b32_e32 v36, 16, v95
	v_and_b32_e32 v37, 0xffff0000, v95
	v_lshl_add_u64 v[30:31], s[26:27], 0, v[30:31]
	v_rcp_f32_e32 v24, v24
	v_rcp_f32_e32 v25, v25
	v_rcp_f32_e32 v18, v18
	v_rcp_f32_e32 v19, v19
	v_pk_add_f32 v[20:21], v[20:21], 1.0 op_sel_hi:[1,0]
	v_exp_f32_e32 v12, v12
	v_exp_f32_e32 v13, v13
	v_pk_add_f32 v[8:9], v[8:9], v[72:73]
	v_pk_add_f32 v[6:7], v[6:7], v[70:71]
	v_pk_mul_f32 v[32:33], v[32:33], v[36:37]
	v_lshlrev_b32_e32 v36, 16, v97
	v_and_b32_e32 v37, 0xffff0000, v97
	v_cvt_pk_bf16_f32 v27, v32, v33
	v_lshl_add_u64 v[30:31], v[30:31], 0, v[184:185]
	v_rcp_f32_e32 v20, v20
	v_rcp_f32_e32 v21, v21
	v_pk_add_f32 v[14:15], v[14:15], 1.0 op_sel_hi:[1,0]
	v_pk_add_f32 v[4:5], v[4:5], v[68:69]
	v_pk_add_f32 v[2:3], v[2:3], v[66:67]
	v_pk_mul_f32 v[6:7], v[6:7], s[38:39] op_sel_hi:[1,0]
	v_pk_mul_f32 v[8:9], v[8:9], s[38:39] op_sel_hi:[1,0]
	v_pk_mul_f32 v[36:37], v[28:29], v[36:37]
	v_cvt_pk_bf16_f32 v28, v34, v35
	v_rcp_f32_e32 v14, v14
	v_cvt_pk_bf16_f32 v29, v36, v37
	global_store_dwordx4 v[30:31], v[26:29], off offset:2048
	v_rcp_f32_e32 v15, v15
	v_pk_add_f32 v[10:11], v[10:11], 1.0 op_sel_hi:[1,0]
	s_waitcnt vmcnt(7)
	v_lshlrev_b32_e32 v26, 16, v90
	v_and_b32_e32 v27, 0xffff0000, v90
	v_exp_f32_e32 v6, v6
	v_exp_f32_e32 v7, v7
	v_exp_f32_e32 v8, v8
	v_exp_f32_e32 v9, v9
	v_pk_mul_f32 v[2:3], v[2:3], s[38:39] op_sel_hi:[1,0]
	v_pk_mul_f32 v[4:5], v[4:5], s[38:39] op_sel_hi:[1,0]
	v_lshlrev_b32_e32 v28, 16, v91
	v_and_b32_e32 v29, 0xffff0000, v91
	v_pk_mul_f32 v[22:23], v[22:23], v[26:27]
	v_lshlrev_b32_e32 v26, 16, v92
	v_and_b32_e32 v27, 0xffff0000, v92
	v_pk_add_f32 v[16:17], v[16:17], 1.0 op_sel_hi:[1,0]
	v_rcp_f32_e32 v10, v10
	v_rcp_f32_e32 v11, v11
	v_exp_f32_e32 v2, v2
	v_exp_f32_e32 v3, v3
	v_exp_f32_e32 v4, v4
	v_exp_f32_e32 v5, v5
	v_pk_mul_f32 v[24:25], v[24:25], v[28:29]
	v_lshlrev_b32_e32 v28, 16, v93
	v_and_b32_e32 v29, 0xffff0000, v93
	v_pk_mul_f32 v[26:27], v[18:19], v[26:27]
	v_cvt_pk_bf16_f32 v18, v22, v23
	v_cvt_pk_bf16_f32 v19, v24, v25
	v_rcp_f32_e32 v16, v16
	v_rcp_f32_e32 v17, v17
	v_pk_add_f32 v[12:13], v[12:13], 1.0 op_sel_hi:[1,0]
	v_pk_mul_f32 v[28:29], v[20:21], v[28:29]
	v_cvt_pk_bf16_f32 v20, v26, v27
	v_rcp_f32_e32 v12, v12
	v_cvt_pk_bf16_f32 v21, v28, v29
	global_store_dwordx4 v[30:31], v[18:21], off offset:2304
	v_rcp_f32_e32 v13, v13
	v_pk_add_f32 v[6:7], v[6:7], 1.0 op_sel_hi:[1,0]
	s_waitcnt vmcnt(7)
	v_lshlrev_b32_e32 v18, 16, v78
	v_and_b32_e32 v19, 0xffff0000, v78
	v_pk_mul_f32 v[14:15], v[14:15], v[18:19]
	v_lshlrev_b32_e32 v18, 16, v80
	v_and_b32_e32 v19, 0xffff0000, v80
	v_pk_add_f32 v[8:9], v[8:9], 1.0 op_sel_hi:[1,0]
	v_lshlrev_b32_e32 v20, 16, v79
	v_and_b32_e32 v21, 0xffff0000, v79
	v_pk_mul_f32 v[18:19], v[10:11], v[18:19]
	v_cvt_pk_bf16_f32 v10, v14, v15
	v_lshlrev_b64 v[14:15], 12, v[106:107]
	v_rcp_f32_e32 v6, v6
	v_rcp_f32_e32 v7, v7
	v_rcp_f32_e32 v8, v8
	v_rcp_f32_e32 v9, v9
	v_pk_add_f32 v[2:3], v[2:3], 1.0 op_sel_hi:[1,0]
	v_pk_add_f32 v[4:5], v[4:5], 1.0 op_sel_hi:[1,0]
	v_pk_mul_f32 v[16:17], v[16:17], v[20:21]
	v_lshlrev_b32_e32 v20, 16, v81
	v_and_b32_e32 v21, 0xffff0000, v81
	v_lshl_add_u64 v[14:15], s[26:27], 0, v[14:15]
	v_rcp_f32_e32 v2, v2
	v_rcp_f32_e32 v3, v3
	v_rcp_f32_e32 v4, v4
	v_rcp_f32_e32 v5, v5
	v_pk_mul_f32 v[20:21], v[12:13], v[20:21]
	v_cvt_pk_bf16_f32 v11, v16, v17
	v_cvt_pk_bf16_f32 v12, v18, v19
	v_lshl_add_u64 v[14:15], v[14:15], 0, v[184:185]
	v_cvt_pk_bf16_f32 v13, v20, v21
	global_store_dwordx4 v[14:15], v[10:13], off offset:2048
	s_waitcnt vmcnt(7)
	s_nop 0
	v_lshlrev_b32_e32 v10, 16, v74
	v_and_b32_e32 v11, 0xffff0000, v74
	v_lshlrev_b32_e32 v12, 16, v75
	v_and_b32_e32 v13, 0xffff0000, v75
	v_pk_mul_f32 v[6:7], v[6:7], v[10:11]
	v_pk_mul_f32 v[8:9], v[8:9], v[12:13]
	v_lshlrev_b32_e32 v10, 16, v76
	v_and_b32_e32 v11, 0xffff0000, v76
	v_lshlrev_b32_e32 v12, 16, v77
	v_and_b32_e32 v13, 0xffff0000, v77
	v_pk_mul_f32 v[10:11], v[2:3], v[10:11]
	v_pk_mul_f32 v[12:13], v[4:5], v[12:13]
	v_cvt_pk_bf16_f32 v2, v6, v7
	v_cvt_pk_bf16_f32 v3, v8, v9
	v_cvt_pk_bf16_f32 v4, v10, v11
	s_nop 0
	v_cvt_pk_bf16_f32 v5, v12, v13
	global_store_dwordx4 v[14:15], v[2:5], off offset:2304
	s_cbranch_vccnz .LBB0_1184
	s_andn2_b64 vcc, exec, s[14:15]
	s_cbranch_vccnz .LBB0_1183
	s_barrier
	s_branch .LBB0_1183

.LBB0_1274:
	v_lshl_or_b32 v144, s2, 8, v157
	v_lshl_add_u32 v154, s56, 8, v1
	v_ashrrev_i32_e32 v145, 31, v144
	v_lshlrev_b64 v[144:145], 2, v[144:145]
	v_ashrrev_i32_e32 v155, 31, v154
	v_lshl_add_u64 v[146:147], s[78:79], 0, v[144:145]
	v_lshlrev_b64 v[148:149], 13, v[154:155]
	v_or_b32_e32 v174, 16, v154
	v_lshl_add_u64 v[170:171], v[146:147], 0, v[148:149]
	v_ashrrev_i32_e32 v175, 31, v174
	global_load_dwordx4 v[150:153], v[170:171], off
	global_load_dwordx4 v[162:165], v[170:171], off offset:64
	global_load_dwordx4 v[166:169], v[170:171], off offset:512
	s_nop 0
	global_load_dwordx4 v[170:173], v[170:171], off offset:576
	v_lshlrev_b64 v[224:225], 13, v[174:175]
	v_or_b32_e32 v190, 32, v154
	v_lshl_add_u64 v[186:187], v[146:147], 0, v[224:225]
	v_ashrrev_i32_e32 v191, 31, v190
	global_load_dwordx4 v[174:177], v[186:187], off
	global_load_dwordx4 v[178:181], v[186:187], off offset:64
	global_load_dwordx4 v[182:185], v[186:187], off offset:512
	s_nop 0
	global_load_dwordx4 v[186:189], v[186:187], off offset:576
	v_lshlrev_b64 v[226:227], 13, v[190:191]
	v_or_b32_e32 v154, 48, v154
	v_lshl_add_u64 v[202:203], v[146:147], 0, v[226:227]
	v_ashrrev_i32_e32 v155, 31, v154
	global_load_dwordx4 v[190:193], v[202:203], off
	global_load_dwordx4 v[194:197], v[202:203], off offset:64
	global_load_dwordx4 v[198:201], v[202:203], off offset:512
	s_nop 0
	global_load_dwordx4 v[202:205], v[202:203], off offset:576
	v_lshlrev_b64 v[154:155], 13, v[154:155]
	v_lshl_add_u64 v[220:221], v[146:147], 0, v[154:155]
	global_load_dwordx4 v[206:209], v[220:221], off
	global_load_dwordx4 v[210:213], v[220:221], off offset:64
	global_load_dwordx4 v[214:217], v[220:221], off offset:512
	s_nop 0
	global_load_dwordx4 v[220:223], v[220:221], off offset:576
	s_mov_b64 s[56:57], -1
	s_andn2_b64 vcc, exec, s[0:1]
	s_waitcnt vmcnt(0)
	v_pk_add_f32 v[126:127], v[126:127], v[150:151]
	v_lshl_add_u64 v[150:151], s[78:79], 0, v[148:149]
	v_lshl_add_u64 v[150:151], v[150:151], 0, v[144:145]
	v_pk_add_f32 v[112:113], v[112:113], v[168:169]
	v_pk_add_f32 v[110:111], v[110:111], v[166:167]
	global_store_dwordx4 v[150:151], v[110:113], off offset:512
	v_pk_add_f32 v[104:105], v[104:105], v[172:173]
	v_pk_add_f32 v[96:97], v[96:97], v[184:185]
	v_lshl_add_u64 v[110:111], s[78:79], 0, v[224:225]
	v_lshl_add_u64 v[110:111], v[110:111], 0, v[144:145]
	v_pk_add_f32 v[94:95], v[94:95], v[182:183]
	global_store_dwordx4 v[110:111], v[94:97], off offset:512
	v_pk_add_f32 v[80:81], v[80:81], v[200:201]
	v_pk_add_f32 v[78:79], v[78:79], v[198:199]
	v_lshl_add_u64 v[94:95], s[78:79], 0, v[226:227]
	v_lshl_add_u64 v[94:95], v[94:95], 0, v[144:145]
	v_pk_add_f32 v[102:103], v[102:103], v[170:171]
	v_pk_add_f32 v[88:89], v[88:89], v[188:189]
	v_pk_add_f32 v[86:87], v[86:87], v[186:187]
	global_store_dwordx4 v[94:95], v[78:81], off offset:512
	v_pk_add_f32 v[76:77], v[76:77], v[204:205]
	v_pk_add_f32 v[74:75], v[74:75], v[202:203]
	v_lshl_add_u64 v[78:79], s[78:79], 0, v[154:155]
	global_store_dwordx4 v[150:151], v[102:105], off offset:576
	global_store_dwordx4 v[110:111], v[86:89], off offset:576
	global_store_dwordx4 v[94:95], v[74:77], off offset:576
	v_pk_add_f32 v[104:105], v[120:121], v[176:177]
	v_pk_add_f32 v[102:103], v[118:119], v[174:175]
	v_pk_add_f32 v[88:89], v[108:109], v[192:193]
	v_pk_add_f32 v[86:87], v[106:107], v[190:191]
	v_pk_add_f32 v[76:77], v[92:93], v[208:209]
	v_pk_add_f32 v[74:75], v[90:91], v[206:207]
	v_lshl_add_u64 v[78:79], v[78:79], 0, v[144:145]
	v_pk_add_f32 v[128:129], v[128:129], v[152:153]
	v_pk_add_f32 v[124:125], v[124:125], v[164:165]
	v_pk_add_f32 v[122:123], v[122:123], v[162:163]
	global_store_dwordx4 v[110:111], v[102:105], off
	global_store_dwordx4 v[94:95], v[86:89], off
	global_store_dwordx4 v[78:79], v[74:77], off
	v_pk_add_f32 v[104:105], v[116:117], v[180:181]
	v_pk_add_f32 v[102:103], v[114:115], v[178:179]
	v_pk_add_f32 v[88:89], v[100:101], v[196:197]
	v_pk_add_f32 v[86:87], v[98:99], v[194:195]
	v_pk_add_f32 v[76:77], v[84:85], v[212:213]
	v_pk_add_f32 v[74:75], v[82:83], v[210:211]
	v_pk_add_f32 v[72:73], v[72:73], v[216:217]
	v_pk_add_f32 v[70:71], v[70:71], v[214:215]
	v_pk_add_f32 v[68:69], v[68:69], v[222:223]
	v_pk_add_f32 v[66:67], v[66:67], v[220:221]
	v_lshl_add_u64 v[154:155], v[148:149], 0, s[36:37]
	global_store_dwordx4 v[150:151], v[126:129], off
	global_store_dwordx4 v[150:151], v[122:125], off offset:64
	global_store_dwordx4 v[110:111], v[102:105], off offset:64
	global_store_dwordx4 v[94:95], v[86:89], off offset:64
	global_store_dwordx4 v[78:79], v[74:77], off offset:64
	global_store_dwordx4 v[78:79], v[70:73], off offset:512
	global_store_dwordx4 v[78:79], v[66:69], off offset:576
	s_setprio 0
	v_lshl_add_u64 v[152:153], v[148:149], 0, s[38:39]
	v_lshl_add_u64 v[150:151], v[148:149], 0, s[40:41]
	v_lshl_add_u64 v[66:67], v[146:147], 0, v[154:155]
	global_load_dwordx4 v[118:121], v[66:67], off
	global_load_dwordx4 v[106:109], v[66:67], off offset:64
	global_load_dwordx4 v[102:105], v[66:67], off offset:512
	global_load_dwordx4 v[94:97], v[66:67], off offset:576
	v_lshl_add_u64 v[66:67], v[146:147], 0, v[152:153]
	global_load_dwordx4 v[98:101], v[66:67], off
	global_load_dwordx4 v[90:93], v[66:67], off offset:64
	global_load_dwordx4 v[82:85], v[66:67], off offset:512
	global_load_dwordx4 v[78:81], v[66:67], off offset:576
	v_lshl_add_u64 v[66:67], v[146:147], 0, v[150:151]
	global_load_dwordx4 v[86:89], v[66:67], off
	global_load_dwordx4 v[74:77], v[66:67], off offset:64
	global_load_dwordx4 v[70:73], v[66:67], off offset:512
	s_nop 0
	global_load_dwordx4 v[66:69], v[66:67], off offset:576
	v_lshl_add_u64 v[148:149], v[148:149], 0, s[42:43]
	v_lshl_add_u64 v[126:127], v[146:147], 0, v[148:149]
	global_load_dwordx4 v[122:125], v[126:127], off
	global_load_dwordx4 v[114:117], v[126:127], off offset:64
	global_load_dwordx4 v[110:113], v[126:127], off offset:512
	s_nop 0
	global_load_dwordx4 v[126:129], v[126:127], off offset:576
	s_waitcnt vmcnt(15)
	v_pk_add_f32 v[62:63], v[62:63], v[118:119]
	v_lshl_add_u64 v[118:119], s[78:79], 0, v[154:155]
	v_lshl_add_u64 v[118:119], v[118:119], 0, v[144:145]
	s_waitcnt vmcnt(13)
	v_pk_add_f32 v[52:53], v[52:53], v[104:105]
	v_pk_add_f32 v[50:51], v[50:51], v[102:103]
	global_store_dwordx4 v[118:119], v[50:53], off offset:512
	s_waitcnt vmcnt(10)
	v_pk_add_f32 v[36:37], v[36:37], v[84:85]
	v_pk_add_f32 v[34:35], v[34:35], v[82:83]
	v_lshl_add_u64 v[50:51], s[78:79], 0, v[152:153]
	v_lshl_add_u64 v[50:51], v[50:51], 0, v[144:145]
	global_store_dwordx4 v[50:51], v[34:37], off offset:512
	s_waitcnt vmcnt(7)
	v_pk_add_f32 v[20:21], v[20:21], v[72:73]
	v_pk_add_f32 v[18:19], v[18:19], v[70:71]
	v_lshl_add_u64 v[34:35], s[78:79], 0, v[150:151]
	v_lshl_add_u64 v[34:35], v[34:35], 0, v[144:145]
	v_pk_add_f32 v[44:45], v[44:45], v[96:97]
	v_pk_add_f32 v[42:43], v[42:43], v[94:95]
	v_pk_add_f32 v[28:29], v[28:29], v[80:81]
	v_pk_add_f32 v[26:27], v[26:27], v[78:79]
	global_store_dwordx4 v[34:35], v[18:21], off offset:512
	s_waitcnt vmcnt(7)
	v_pk_add_f32 v[12:13], v[12:13], v[68:69]
	v_pk_add_f32 v[10:11], v[10:11], v[66:67]
	v_lshl_add_u64 v[18:19], s[78:79], 0, v[148:149]
	global_store_dwordx4 v[118:119], v[42:45], off offset:576
	global_store_dwordx4 v[50:51], v[26:29], off offset:576
	global_store_dwordx4 v[34:35], v[10:13], off offset:576
	v_pk_add_f32 v[44:45], v[56:57], v[100:101]
	v_pk_add_f32 v[42:43], v[54:55], v[98:99]
	v_pk_add_f32 v[28:29], v[40:41], v[88:89]
	v_pk_add_f32 v[26:27], v[38:39], v[86:87]
	s_waitcnt vmcnt(9)
	v_pk_add_f32 v[12:13], v[24:25], v[124:125]
	v_pk_add_f32 v[10:11], v[22:23], v[122:123]
	v_lshl_add_u64 v[18:19], v[18:19], 0, v[144:145]
	v_pk_add_f32 v[64:65], v[64:65], v[120:121]
	v_pk_add_f32 v[60:61], v[60:61], v[108:109]
	v_pk_add_f32 v[58:59], v[58:59], v[106:107]
	global_store_dwordx4 v[50:51], v[42:45], off
	global_store_dwordx4 v[34:35], v[26:29], off
	global_store_dwordx4 v[18:19], v[10:13], off
	v_pk_add_f32 v[44:45], v[48:49], v[92:93]
	v_pk_add_f32 v[42:43], v[46:47], v[90:91]
	v_pk_add_f32 v[28:29], v[32:33], v[76:77]
	v_pk_add_f32 v[26:27], v[30:31], v[74:75]
	s_waitcnt vmcnt(11)
	v_pk_add_f32 v[12:13], v[16:17], v[116:117]
	v_pk_add_f32 v[10:11], v[14:15], v[114:115]
	s_waitcnt vmcnt(10)
	v_pk_add_f32 v[8:9], v[8:9], v[112:113]
	v_pk_add_f32 v[6:7], v[6:7], v[110:111]
	s_waitcnt vmcnt(9)
	v_pk_add_f32 v[4:5], v[4:5], v[128:129]
	v_pk_add_f32 v[2:3], v[2:3], v[126:127]
	global_store_dwordx4 v[118:119], v[62:65], off
	global_store_dwordx4 v[118:119], v[58:61], off offset:64
	global_store_dwordx4 v[50:51], v[42:45], off offset:64
	global_store_dwordx4 v[34:35], v[26:29], off offset:64
	global_store_dwordx4 v[18:19], v[10:13], off offset:64
	global_store_dwordx4 v[18:19], v[6:9], off offset:512
	global_store_dwordx4 v[18:19], v[2:5], off offset:576
	s_cbranch_vccnz .LBB0_1263
	s_andn2_b64 vcc, exec, s[12:13]
	s_cbranch_vccnz .LBB0_1262
	s_barrier
	s_branch .LBB0_1262

.LBB0_1500:
	v_pk_mul_f32 v[10:11], v[160:161], s[42:43] op_sel_hi:[1,0]
	v_pk_mul_f32 v[8:9], v[158:159], s[42:43] op_sel_hi:[1,0]
	v_exp_f32_e32 v10, v10
	v_exp_f32_e32 v11, v11
	v_exp_f32_e32 v8, v8
	v_exp_f32_e32 v9, v9
	v_pk_mul_f32 v[12:13], v[160:161], v[156:157]
	v_pk_fma_f32 v[10:11], v[10:11], s[44:45], s[44:45] op_sel_hi:[1,0,0]
	v_pk_mul_f32 v[14:15], v[158:159], v[154:155]
	v_rcp_f32_e32 v10, v10
	v_rcp_f32_e32 v11, v11
	v_pk_fma_f32 v[8:9], v[8:9], s[44:45], s[44:45] op_sel_hi:[1,0,0]
	v_pk_mul_f32 v[18:19], v[150:151], v[146:147]
	v_rcp_f32_e32 v8, v8
	v_rcp_f32_e32 v9, v9
	v_pk_mul_f32 v[10:11], v[12:13], v[10:11]
	v_pk_mul_f32 v[12:13], v[150:151], s[42:43] op_sel_hi:[1,0]
	v_pk_mul_f32 v[16:17], v[152:153], v[148:149]
	v_exp_f32_e32 v12, v12
	v_exp_f32_e32 v13, v13
	v_pk_mul_f32 v[8:9], v[14:15], v[8:9]
	v_pk_mul_f32 v[14:15], v[152:153], s[42:43] op_sel_hi:[1,0]
	v_med3_f32 v7, v8, s72, v191
	v_exp_f32_e32 v14, v14
	v_exp_f32_e32 v15, v15
	v_pk_fma_f32 v[12:13], v[12:13], s[44:45], s[44:45] op_sel_hi:[1,0,0]
	v_med3_f32 v9, v9, s72, v191
	v_rcp_f32_e32 v12, v12
	v_rcp_f32_e32 v13, v13
	v_pk_fma_f32 v[14:15], v[14:15], s[44:45], s[44:45] op_sel_hi:[1,0,0]
	v_rcp_f32_e32 v14, v14
	v_rcp_f32_e32 v15, v15
	v_pk_mul_f32 v[12:13], v[18:19], v[12:13]
	v_cvt_pk_fp8_f32 v8, v7, v9
	v_med3_f32 v7, v10, s72, v191
	v_med3_f32 v10, v11, s72, v191
	v_med3_f32 v11, v12, s72, v191
	v_med3_f32 v12, v13, s72, v191
	v_cvt_pk_fp8_f32 v9, v11, v12
	v_pk_mul_f32 v[14:15], v[16:17], v[14:15]
	v_readlane_b32 s4, v254, 56
	v_cvt_pk_fp8_f32 v8, v7, v10 op_sel:[0,0,1]
	v_med3_f32 v7, v14, s72, v191
	v_med3_f32 v10, v15, s72, v191
	v_readlane_b32 s5, v254, 57
	v_cvt_pk_fp8_f32 v9, v7, v10 op_sel:[0,0,1]
	v_lshl_add_u32 v6, s54, 8, v1
	v_lshl_or_b32 v2, s52, 7, v185
	v_mov_b64_e32 v[4:5], s[4:5]
	v_ashrrev_i32_e32 v3, 31, v2
	v_mad_i64_i32 v[10:11], s[4:5], v6, s71, v[4:5]
	v_lshl_add_u64 v[10:11], v[10:11], 0, v[2:3]
	s_nop 15
	s_nop 15
	global_store_dwordx2 v[10:11], v[8:9], off
	v_pk_mul_f32 v[8:9], v[142:143], s[42:43] op_sel_hi:[1,0]
	v_pk_mul_f32 v[10:11], v[144:145], s[42:43] op_sel_hi:[1,0]
	v_exp_f32_e32 v8, v8
	v_exp_f32_e32 v9, v9
	v_exp_f32_e32 v10, v10
	v_exp_f32_e32 v11, v11
	v_pk_mul_f32 v[12:13], v[144:145], v[140:141]
	v_pk_fma_f32 v[8:9], v[8:9], s[44:45], s[44:45] op_sel_hi:[1,0,0]
	v_pk_mul_f32 v[14:15], v[142:143], v[138:139]
	v_pk_fma_f32 v[10:11], v[10:11], s[44:45], s[44:45] op_sel_hi:[1,0,0]
	v_rcp_f32_e32 v8, v8
	v_rcp_f32_e32 v9, v9
	v_rcp_f32_e32 v10, v10
	v_rcp_f32_e32 v11, v11
	v_pk_mul_f32 v[16:17], v[136:137], v[132:133]
	v_pk_mul_f32 v[8:9], v[14:15], v[8:9]
	v_pk_mul_f32 v[14:15], v[136:137], s[42:43] op_sel_hi:[1,0]
	v_pk_mul_f32 v[10:11], v[12:13], v[10:11]
	v_pk_mul_f32 v[12:13], v[134:135], s[42:43] op_sel_hi:[1,0]
	v_exp_f32_e32 v14, v14
	v_exp_f32_e32 v12, v12
	v_exp_f32_e32 v13, v13
	v_exp_f32_e32 v15, v15
	v_pk_mul_f32 v[18:19], v[134:135], v[130:131]
	v_med3_f32 v9, v9, s72, v191
	v_pk_fma_f32 v[12:13], v[12:13], s[44:45], s[44:45] op_sel_hi:[1,0,0]
	v_pk_fma_f32 v[14:15], v[14:15], s[44:45], s[44:45] op_sel_hi:[1,0,0]
	v_rcp_f32_e32 v12, v12
	v_rcp_f32_e32 v13, v13
	v_rcp_f32_e32 v14, v14
	v_rcp_f32_e32 v15, v15
	v_med3_f32 v10, v10, s72, v191
	v_pk_mul_f32 v[12:13], v[18:19], v[12:13]
	v_med3_f32 v11, v11, s72, v191
	v_pk_mul_f32 v[14:15], v[16:17], v[14:15]
	v_med3_f32 v16, v8, s72, v191
	v_cvt_pk_fp8_f32 v8, v16, v9
	v_med3_f32 v12, v12, s72, v191
	v_med3_f32 v13, v13, s72, v191
	v_cvt_pk_fp8_f32 v9, v12, v13
	v_cvt_pk_fp8_f32 v8, v10, v11 op_sel:[0,0,1]
	v_med3_f32 v10, v14, s72, v191
	v_med3_f32 v11, v15, s72, v191
	v_cvt_pk_fp8_f32 v9, v10, v11 op_sel:[0,0,1]
	v_or_b32_e32 v7, 16, v6
	v_mad_i64_i32 v[10:11], s[4:5], v7, s71, v[4:5]
	v_lshl_add_u64 v[10:11], v[10:11], 0, v[2:3]
	global_store_dwordx2 v[10:11], v[8:9], off
	v_pk_mul_f32 v[8:9], v[126:127], s[42:43] op_sel_hi:[1,0]
	v_pk_mul_f32 v[10:11], v[128:129], s[42:43] op_sel_hi:[1,0]
	v_exp_f32_e32 v8, v8
	v_exp_f32_e32 v9, v9
	v_exp_f32_e32 v10, v10
	v_exp_f32_e32 v11, v11
	v_pk_mul_f32 v[12:13], v[128:129], v[124:125]
	v_pk_fma_f32 v[8:9], v[8:9], s[44:45], s[44:45] op_sel_hi:[1,0,0]
	v_pk_mul_f32 v[14:15], v[126:127], v[122:123]
	v_pk_fma_f32 v[10:11], v[10:11], s[44:45], s[44:45] op_sel_hi:[1,0,0]
	v_rcp_f32_e32 v8, v8
	v_rcp_f32_e32 v9, v9
	v_rcp_f32_e32 v10, v10
	v_rcp_f32_e32 v11, v11
	v_pk_mul_f32 v[16:17], v[120:121], v[116:117]
	v_pk_mul_f32 v[8:9], v[14:15], v[8:9]
	v_pk_mul_f32 v[14:15], v[120:121], s[42:43] op_sel_hi:[1,0]
	v_pk_mul_f32 v[10:11], v[12:13], v[10:11]
	v_pk_mul_f32 v[12:13], v[118:119], s[42:43] op_sel_hi:[1,0]
	v_exp_f32_e32 v14, v14
	v_exp_f32_e32 v12, v12
	v_exp_f32_e32 v13, v13
	v_exp_f32_e32 v15, v15
	v_pk_mul_f32 v[18:19], v[118:119], v[114:115]
	v_med3_f32 v9, v9, s72, v191
	v_pk_fma_f32 v[12:13], v[12:13], s[44:45], s[44:45] op_sel_hi:[1,0,0]
	v_pk_fma_f32 v[14:15], v[14:15], s[44:45], s[44:45] op_sel_hi:[1,0,0]
	v_rcp_f32_e32 v12, v12
	v_rcp_f32_e32 v13, v13
	v_rcp_f32_e32 v14, v14
	v_rcp_f32_e32 v15, v15
	v_med3_f32 v10, v10, s72, v191
	v_pk_mul_f32 v[12:13], v[18:19], v[12:13]
	v_med3_f32 v11, v11, s72, v191
	v_pk_mul_f32 v[14:15], v[16:17], v[14:15]
	v_med3_f32 v16, v8, s72, v191
	v_cvt_pk_fp8_f32 v8, v16, v9
	v_med3_f32 v12, v12, s72, v191
	v_med3_f32 v13, v13, s72, v191
	v_cvt_pk_fp8_f32 v9, v12, v13
	v_cvt_pk_fp8_f32 v8, v10, v11 op_sel:[0,0,1]
	v_med3_f32 v10, v14, s72, v191
	v_med3_f32 v11, v15, s72, v191
	v_cvt_pk_fp8_f32 v9, v10, v11 op_sel:[0,0,1]
	v_or_b32_e32 v7, 32, v6
	v_mad_i64_i32 v[10:11], s[4:5], v7, s71, v[4:5]
	v_lshl_add_u64 v[10:11], v[10:11], 0, v[2:3]
	global_store_dwordx2 v[10:11], v[8:9], off
	v_pk_mul_f32 v[8:9], v[110:111], s[42:43] op_sel_hi:[1,0]
	v_pk_mul_f32 v[10:11], v[112:113], s[42:43] op_sel_hi:[1,0]
	v_exp_f32_e32 v8, v8
	v_exp_f32_e32 v9, v9
	v_exp_f32_e32 v10, v10
	v_exp_f32_e32 v11, v11
	v_pk_mul_f32 v[12:13], v[112:113], v[108:109]
	v_pk_fma_f32 v[8:9], v[8:9], s[44:45], s[44:45] op_sel_hi:[1,0,0]
	v_pk_mul_f32 v[14:15], v[110:111], v[106:107]
	v_pk_fma_f32 v[10:11], v[10:11], s[44:45], s[44:45] op_sel_hi:[1,0,0]
	v_rcp_f32_e32 v8, v8
	v_rcp_f32_e32 v9, v9
	v_rcp_f32_e32 v10, v10
	v_rcp_f32_e32 v11, v11
	v_pk_mul_f32 v[16:17], v[104:105], v[100:101]
	v_pk_mul_f32 v[8:9], v[14:15], v[8:9]
	v_pk_mul_f32 v[14:15], v[104:105], s[42:43] op_sel_hi:[1,0]
	v_pk_mul_f32 v[10:11], v[12:13], v[10:11]
	v_pk_mul_f32 v[12:13], v[102:103], s[42:43] op_sel_hi:[1,0]
	v_exp_f32_e32 v14, v14
	v_exp_f32_e32 v12, v12
	v_exp_f32_e32 v13, v13
	v_exp_f32_e32 v15, v15
	v_pk_mul_f32 v[18:19], v[102:103], v[98:99]
	v_med3_f32 v9, v9, s72, v191
	v_pk_fma_f32 v[12:13], v[12:13], s[44:45], s[44:45] op_sel_hi:[1,0,0]
	v_pk_fma_f32 v[14:15], v[14:15], s[44:45], s[44:45] op_sel_hi:[1,0,0]
	v_rcp_f32_e32 v12, v12
	v_rcp_f32_e32 v13, v13
	v_rcp_f32_e32 v14, v14
	v_rcp_f32_e32 v15, v15
	v_med3_f32 v10, v10, s72, v191
	v_pk_mul_f32 v[12:13], v[18:19], v[12:13]
	v_med3_f32 v11, v11, s72, v191
	v_pk_mul_f32 v[14:15], v[16:17], v[14:15]
	v_med3_f32 v16, v8, s72, v191
	v_cvt_pk_fp8_f32 v8, v16, v9
	v_med3_f32 v12, v12, s72, v191
	v_med3_f32 v13, v13, s72, v191
	v_cvt_pk_fp8_f32 v9, v12, v13
	v_cvt_pk_fp8_f32 v8, v10, v11 op_sel:[0,0,1]
	v_med3_f32 v10, v14, s72, v191
	v_med3_f32 v11, v15, s72, v191
	v_cvt_pk_fp8_f32 v9, v10, v11 op_sel:[0,0,1]
	v_or_b32_e32 v7, 48, v6
	v_mad_i64_i32 v[10:11], s[4:5], v7, s71, v[4:5]
	v_lshl_add_u64 v[10:11], v[10:11], 0, v[2:3]
	global_store_dwordx2 v[10:11], v[8:9], off
	s_setprio 0
	v_pk_mul_f32 v[8:9], v[94:95], s[42:43] op_sel_hi:[1,0]
	v_pk_mul_f32 v[10:11], v[96:97], s[42:43] op_sel_hi:[1,0]
	v_exp_f32_e32 v8, v8
	v_exp_f32_e32 v9, v9
	v_exp_f32_e32 v10, v10
	v_exp_f32_e32 v11, v11
	v_pk_mul_f32 v[12:13], v[96:97], v[92:93]
	v_pk_fma_f32 v[8:9], v[8:9], s[44:45], s[44:45] op_sel_hi:[1,0,0]
	v_pk_mul_f32 v[14:15], v[94:95], v[90:91]
	v_pk_fma_f32 v[10:11], v[10:11], s[44:45], s[44:45] op_sel_hi:[1,0,0]
	v_rcp_f32_e32 v8, v8
	v_rcp_f32_e32 v9, v9
	v_rcp_f32_e32 v10, v10
	v_rcp_f32_e32 v11, v11
	v_pk_mul_f32 v[16:17], v[88:89], v[84:85]
	v_pk_mul_f32 v[8:9], v[14:15], v[8:9]
	v_pk_mul_f32 v[14:15], v[88:89], s[42:43] op_sel_hi:[1,0]
	v_pk_mul_f32 v[10:11], v[12:13], v[10:11]
	v_pk_mul_f32 v[12:13], v[86:87], s[42:43] op_sel_hi:[1,0]
	v_exp_f32_e32 v14, v14
	v_exp_f32_e32 v12, v12
	v_exp_f32_e32 v13, v13
	v_exp_f32_e32 v15, v15
	v_pk_mul_f32 v[18:19], v[86:87], v[82:83]
	v_med3_f32 v9, v9, s72, v191
	v_pk_fma_f32 v[12:13], v[12:13], s[44:45], s[44:45] op_sel_hi:[1,0,0]
	v_pk_fma_f32 v[14:15], v[14:15], s[44:45], s[44:45] op_sel_hi:[1,0,0]
	v_rcp_f32_e32 v12, v12
	v_rcp_f32_e32 v13, v13
	v_rcp_f32_e32 v14, v14
	v_rcp_f32_e32 v15, v15
	v_med3_f32 v10, v10, s72, v191
	v_pk_mul_f32 v[12:13], v[18:19], v[12:13]
	v_med3_f32 v11, v11, s72, v191
	v_pk_mul_f32 v[14:15], v[16:17], v[14:15]
	v_med3_f32 v16, v8, s72, v191
	v_cvt_pk_fp8_f32 v8, v16, v9
	v_med3_f32 v12, v12, s72, v191
	v_med3_f32 v13, v13, s72, v191
	v_cvt_pk_fp8_f32 v9, v12, v13
	v_cvt_pk_fp8_f32 v8, v10, v11 op_sel:[0,0,1]
	v_med3_f32 v10, v14, s72, v191
	v_med3_f32 v11, v15, s72, v191
	v_cvt_pk_fp8_f32 v9, v10, v11 op_sel:[0,0,1]
	v_add_u32_e32 v7, 0x80, v6
	v_mad_i64_i32 v[10:11], s[4:5], v7, s71, v[4:5]
	v_lshl_add_u64 v[10:11], v[10:11], 0, v[2:3]
	global_store_dwordx2 v[10:11], v[8:9], off
	v_pk_mul_f32 v[8:9], v[78:79], s[42:43] op_sel_hi:[1,0]
	v_pk_mul_f32 v[10:11], v[80:81], s[42:43] op_sel_hi:[1,0]
	v_exp_f32_e32 v8, v8
	v_exp_f32_e32 v9, v9
	v_exp_f32_e32 v10, v10
	v_exp_f32_e32 v11, v11
	v_pk_mul_f32 v[12:13], v[80:81], v[76:77]
	v_pk_fma_f32 v[8:9], v[8:9], s[44:45], s[44:45] op_sel_hi:[1,0,0]
	v_pk_mul_f32 v[14:15], v[78:79], v[74:75]
	v_pk_fma_f32 v[10:11], v[10:11], s[44:45], s[44:45] op_sel_hi:[1,0,0]
	v_rcp_f32_e32 v8, v8
	v_rcp_f32_e32 v9, v9
	v_rcp_f32_e32 v10, v10
	v_rcp_f32_e32 v11, v11
	v_pk_mul_f32 v[16:17], v[72:73], v[68:69]
	v_pk_mul_f32 v[8:9], v[14:15], v[8:9]
	v_pk_mul_f32 v[14:15], v[72:73], s[42:43] op_sel_hi:[1,0]
	v_pk_mul_f32 v[10:11], v[12:13], v[10:11]
	v_pk_mul_f32 v[12:13], v[70:71], s[42:43] op_sel_hi:[1,0]
	v_exp_f32_e32 v14, v14
	v_exp_f32_e32 v12, v12
	v_exp_f32_e32 v13, v13
	v_exp_f32_e32 v15, v15
	v_pk_mul_f32 v[18:19], v[70:71], v[66:67]
	v_med3_f32 v9, v9, s72, v191
	v_pk_fma_f32 v[12:13], v[12:13], s[44:45], s[44:45] op_sel_hi:[1,0,0]
	v_pk_fma_f32 v[14:15], v[14:15], s[44:45], s[44:45] op_sel_hi:[1,0,0]
	v_rcp_f32_e32 v12, v12
	v_rcp_f32_e32 v13, v13
	v_rcp_f32_e32 v14, v14
	v_rcp_f32_e32 v15, v15
	v_med3_f32 v10, v10, s72, v191
	v_pk_mul_f32 v[12:13], v[18:19], v[12:13]
	v_med3_f32 v11, v11, s72, v191
	v_pk_mul_f32 v[14:15], v[16:17], v[14:15]
	v_med3_f32 v16, v8, s72, v191
	v_cvt_pk_fp8_f32 v8, v16, v9
	v_med3_f32 v12, v12, s72, v191
	v_med3_f32 v13, v13, s72, v191
	v_cvt_pk_fp8_f32 v9, v12, v13
	v_cvt_pk_fp8_f32 v8, v10, v11 op_sel:[0,0,1]
	v_med3_f32 v10, v14, s72, v191
	v_med3_f32 v11, v15, s72, v191
	v_cvt_pk_fp8_f32 v9, v10, v11 op_sel:[0,0,1]
	v_add_u32_e32 v7, 0x90, v6
	v_mad_i64_i32 v[10:11], s[4:5], v7, s71, v[4:5]
	v_lshl_add_u64 v[10:11], v[10:11], 0, v[2:3]
	global_store_dwordx2 v[10:11], v[8:9], off
	v_pk_mul_f32 v[8:9], v[62:63], s[42:43] op_sel_hi:[1,0]
	v_pk_mul_f32 v[10:11], v[64:65], s[42:43] op_sel_hi:[1,0]
	v_exp_f32_e32 v8, v8
	v_exp_f32_e32 v9, v9
	v_exp_f32_e32 v10, v10
	v_exp_f32_e32 v11, v11
	v_pk_mul_f32 v[12:13], v[64:65], v[60:61]
	v_pk_fma_f32 v[8:9], v[8:9], s[44:45], s[44:45] op_sel_hi:[1,0,0]
	v_pk_mul_f32 v[14:15], v[62:63], v[58:59]
	v_pk_fma_f32 v[10:11], v[10:11], s[44:45], s[44:45] op_sel_hi:[1,0,0]
	v_rcp_f32_e32 v8, v8
	v_rcp_f32_e32 v9, v9
	v_rcp_f32_e32 v10, v10
	v_rcp_f32_e32 v11, v11
	v_pk_mul_f32 v[16:17], v[56:57], v[52:53]
	v_pk_mul_f32 v[8:9], v[14:15], v[8:9]
	v_pk_mul_f32 v[14:15], v[56:57], s[42:43] op_sel_hi:[1,0]
	v_pk_mul_f32 v[10:11], v[12:13], v[10:11]
	v_pk_mul_f32 v[12:13], v[54:55], s[42:43] op_sel_hi:[1,0]
	v_exp_f32_e32 v14, v14
	v_exp_f32_e32 v12, v12
	v_exp_f32_e32 v13, v13
	v_exp_f32_e32 v15, v15
	v_pk_mul_f32 v[18:19], v[54:55], v[50:51]
	v_med3_f32 v9, v9, s72, v191
	v_pk_fma_f32 v[12:13], v[12:13], s[44:45], s[44:45] op_sel_hi:[1,0,0]
	v_pk_fma_f32 v[14:15], v[14:15], s[44:45], s[44:45] op_sel_hi:[1,0,0]
	v_rcp_f32_e32 v12, v12
	v_rcp_f32_e32 v13, v13
	v_rcp_f32_e32 v14, v14
	v_rcp_f32_e32 v15, v15
	v_med3_f32 v10, v10, s72, v191
	v_pk_mul_f32 v[12:13], v[18:19], v[12:13]
	v_med3_f32 v11, v11, s72, v191
	v_pk_mul_f32 v[14:15], v[16:17], v[14:15]
	v_med3_f32 v16, v8, s72, v191
	v_cvt_pk_fp8_f32 v8, v16, v9
	v_med3_f32 v12, v12, s72, v191
	v_med3_f32 v13, v13, s72, v191
	v_cvt_pk_fp8_f32 v9, v12, v13
	v_cvt_pk_fp8_f32 v8, v10, v11 op_sel:[0,0,1]
	v_med3_f32 v10, v14, s72, v191
	v_med3_f32 v11, v15, s72, v191
	v_cvt_pk_fp8_f32 v9, v10, v11 op_sel:[0,0,1]
	v_add_u32_e32 v7, 0xa0, v6
	v_mad_i64_i32 v[10:11], s[4:5], v7, s71, v[4:5]
	v_lshl_add_u64 v[10:11], v[10:11], 0, v[2:3]
	global_store_dwordx2 v[10:11], v[8:9], off
	v_add_u32_e32 v18, 0xb0, v6
	v_pk_mul_f32 v[6:7], v[46:47], s[42:43] op_sel_hi:[1,0]
	v_pk_mul_f32 v[8:9], v[48:49], s[42:43] op_sel_hi:[1,0]
	v_exp_f32_e32 v6, v6
	v_exp_f32_e32 v7, v7
	v_exp_f32_e32 v8, v8
	v_exp_f32_e32 v9, v9
	v_pk_mul_f32 v[10:11], v[48:49], v[44:45]
	v_pk_fma_f32 v[6:7], v[6:7], s[44:45], s[44:45] op_sel_hi:[1,0,0]
	v_pk_mul_f32 v[12:13], v[46:47], v[42:43]
	v_pk_fma_f32 v[8:9], v[8:9], s[44:45], s[44:45] op_sel_hi:[1,0,0]
	v_rcp_f32_e32 v6, v6
	v_rcp_f32_e32 v7, v7
	v_rcp_f32_e32 v8, v8
	v_rcp_f32_e32 v9, v9
	v_pk_mul_f32 v[14:15], v[40:41], v[36:37]
	v_pk_mul_f32 v[6:7], v[12:13], v[6:7]
	v_pk_mul_f32 v[12:13], v[40:41], s[42:43] op_sel_hi:[1,0]
	v_pk_mul_f32 v[8:9], v[10:11], v[8:9]
	v_pk_mul_f32 v[10:11], v[38:39], s[42:43] op_sel_hi:[1,0]
	v_exp_f32_e32 v12, v12
	v_exp_f32_e32 v10, v10
	v_exp_f32_e32 v11, v11
	v_exp_f32_e32 v13, v13
	v_pk_mul_f32 v[16:17], v[38:39], v[34:35]
	v_med3_f32 v7, v7, s72, v191
	v_pk_fma_f32 v[10:11], v[10:11], s[44:45], s[44:45] op_sel_hi:[1,0,0]
	v_pk_fma_f32 v[12:13], v[12:13], s[44:45], s[44:45] op_sel_hi:[1,0,0]
	v_rcp_f32_e32 v10, v10
	v_rcp_f32_e32 v11, v11
	v_rcp_f32_e32 v12, v12
	v_rcp_f32_e32 v13, v13
	v_med3_f32 v8, v8, s72, v191
	v_pk_mul_f32 v[10:11], v[16:17], v[10:11]
	v_med3_f32 v9, v9, s72, v191
	v_pk_mul_f32 v[12:13], v[14:15], v[12:13]
	v_med3_f32 v14, v6, s72, v191
	v_cvt_pk_fp8_f32 v6, v14, v7
	v_med3_f32 v10, v10, s72, v191
	v_med3_f32 v11, v11, s72, v191
	v_cvt_pk_fp8_f32 v7, v10, v11
	v_cvt_pk_fp8_f32 v6, v8, v9 op_sel:[0,0,1]
	v_med3_f32 v8, v12, s72, v191
	v_med3_f32 v9, v13, s72, v191
	v_cvt_pk_fp8_f32 v7, v8, v9 op_sel:[0,0,1]
	v_mad_i64_i32 v[4:5], s[4:5], v18, s71, v[4:5]
	v_lshl_add_u64 v[2:3], v[4:5], 0, v[2:3]
	s_and_b64 vcc, exec, s[0:1]
	s_mov_b64 s[0:1], -1
	global_store_dwordx2 v[2:3], v[6:7], off
	s_cbranch_vccnz .LBB0_1487
	s_andn2_b64 vcc, exec, s[18:19]
	s_cbranch_vccnz .LBB0_1486
	s_barrier
	s_branch .LBB0_1486

.LBB0_1571:
	v_lshl_add_u32 v8, s54, 8, v1
	v_lshl_or_b32 v2, s2, 8, v185
	v_ashrrev_i32_e32 v9, 31, v8
	v_ashrrev_i32_e32 v3, 31, v2
	v_lshlrev_b64 v[4:5], 12, v[8:9]
	v_lshl_add_u64 v[4:5], s[22:23], 0, v[4:5]
	v_lshlrev_b64 v[10:11], 1, v[2:3]
	s_nop 15
	s_nop 15
	v_lshl_add_u64 v[2:3], v[4:5], 0, v[10:11]
	v_cvt_pk_bf16_f32 v4, v158, v159
	v_cvt_pk_bf16_f32 v5, v160, v161
	v_cvt_pk_bf16_f32 v6, v154, v155
	v_cvt_pk_bf16_f32 v7, v156, v157
	global_store_dwordx4 v[2:3], v[4:7], off
	s_nop 1
	v_cvt_pk_bf16_f32 v4, v146, v147
	v_cvt_pk_bf16_f32 v5, v148, v149
	v_cvt_pk_bf16_f32 v6, v138, v139
	v_cvt_pk_bf16_f32 v7, v140, v141
	global_store_dwordx4 v[2:3], v[4:7], off offset:256
	s_nop 1
	v_or_b32_e32 v4, 16, v8
	v_ashrrev_i32_e32 v5, 31, v4
	v_lshlrev_b64 v[4:5], 12, v[4:5]
	v_lshl_add_u64 v[4:5], s[22:23], 0, v[4:5]
	v_lshl_add_u64 v[12:13], v[4:5], 0, v[10:11]
	v_cvt_pk_bf16_f32 v4, v150, v151
	v_cvt_pk_bf16_f32 v5, v152, v153
	v_cvt_pk_bf16_f32 v6, v142, v143
	v_cvt_pk_bf16_f32 v7, v144, v145
	global_store_dwordx4 v[12:13], v[4:7], off
	s_nop 1
	v_cvt_pk_bf16_f32 v4, v130, v131
	v_cvt_pk_bf16_f32 v5, v132, v133
	v_cvt_pk_bf16_f32 v6, v122, v123
	v_cvt_pk_bf16_f32 v7, v124, v125
	global_store_dwordx4 v[12:13], v[4:7], off offset:256
	s_nop 1
	v_or_b32_e32 v4, 32, v8
	v_ashrrev_i32_e32 v5, 31, v4
	v_lshlrev_b64 v[4:5], 12, v[4:5]
	v_lshl_add_u64 v[4:5], s[22:23], 0, v[4:5]
	v_lshl_add_u64 v[12:13], v[4:5], 0, v[10:11]
	v_cvt_pk_bf16_f32 v4, v134, v135
	v_cvt_pk_bf16_f32 v5, v136, v137
	v_cvt_pk_bf16_f32 v6, v126, v127
	v_cvt_pk_bf16_f32 v7, v128, v129
	global_store_dwordx4 v[12:13], v[4:7], off
	s_nop 1
	v_cvt_pk_bf16_f32 v4, v114, v115
	v_cvt_pk_bf16_f32 v5, v116, v117
	v_cvt_pk_bf16_f32 v6, v106, v107
	v_cvt_pk_bf16_f32 v7, v108, v109
	global_store_dwordx4 v[12:13], v[4:7], off offset:256
	s_nop 1
	v_or_b32_e32 v4, 48, v8
	v_ashrrev_i32_e32 v5, 31, v4
	v_lshlrev_b64 v[4:5], 12, v[4:5]
	v_lshl_add_u64 v[4:5], s[22:23], 0, v[4:5]
	v_lshl_add_u64 v[8:9], v[4:5], 0, v[10:11]
	v_cvt_pk_bf16_f32 v4, v118, v119
	v_cvt_pk_bf16_f32 v5, v120, v121
	v_cvt_pk_bf16_f32 v6, v110, v111
	v_cvt_pk_bf16_f32 v7, v112, v113
	global_store_dwordx4 v[8:9], v[4:7], off
	v_add_co_u32_e32 v10, vcc, s71, v2
	s_nop 0
	v_cvt_pk_bf16_f32 v4, v102, v103
	v_cvt_pk_bf16_f32 v5, v104, v105
	v_cvt_pk_bf16_f32 v6, v98, v99
	v_cvt_pk_bf16_f32 v7, v100, v101
	global_store_dwordx4 v[8:9], v[4:7], off offset:256
	s_setprio 0
	v_addc_co_u32_e32 v11, vcc, 0, v3, vcc
	s_nop 0
	v_cvt_pk_bf16_f32 v4, v94, v95
	v_cvt_pk_bf16_f32 v5, v96, v97
	v_cvt_pk_bf16_f32 v6, v90, v91
	v_cvt_pk_bf16_f32 v7, v92, v93
	v_lshl_add_u64 v[8:9], v[2:3], 0, s[46:47]
	global_store_dwordx4 v[10:11], v[4:7], off
	v_add_co_u32_e32 v10, vcc, s72, v2
	s_nop 0
	v_cvt_pk_bf16_f32 v4, v82, v83
	v_cvt_pk_bf16_f32 v5, v84, v85
	v_cvt_pk_bf16_f32 v6, v74, v75
	v_cvt_pk_bf16_f32 v7, v76, v77
	global_store_dwordx4 v[8:9], v[4:7], off offset:256
	v_addc_co_u32_e32 v11, vcc, 0, v3, vcc
	s_nop 0
	v_cvt_pk_bf16_f32 v4, v86, v87
	v_cvt_pk_bf16_f32 v5, v88, v89
	v_cvt_pk_bf16_f32 v6, v78, v79
	v_cvt_pk_bf16_f32 v7, v80, v81
	v_lshl_add_u64 v[8:9], v[2:3], 0, s[48:49]
	global_store_dwordx4 v[10:11], v[4:7], off
	v_add_co_u32_e32 v10, vcc, s73, v2
	s_nop 0
	v_cvt_pk_bf16_f32 v4, v66, v67
	v_cvt_pk_bf16_f32 v5, v68, v69
	v_cvt_pk_bf16_f32 v6, v58, v59
	v_cvt_pk_bf16_f32 v7, v60, v61
	global_store_dwordx4 v[8:9], v[4:7], off offset:256
	v_lshl_add_u64 v[8:9], v[2:3], 0, s[50:51]
	v_addc_co_u32_e32 v11, vcc, 0, v3, vcc
	v_cvt_pk_bf16_f32 v4, v70, v71
	v_cvt_pk_bf16_f32 v5, v72, v73
	v_cvt_pk_bf16_f32 v6, v62, v63
	v_cvt_pk_bf16_f32 v7, v64, v65
	global_store_dwordx4 v[10:11], v[4:7], off
	s_nop 1
	v_cvt_pk_bf16_f32 v4, v50, v51
	v_cvt_pk_bf16_f32 v5, v52, v53
	v_cvt_pk_bf16_f32 v6, v42, v43
	v_cvt_pk_bf16_f32 v7, v44, v45
	global_store_dwordx4 v[8:9], v[4:7], off offset:256
	v_lshl_add_u64 v[8:9], v[2:3], 0, s[20:21]
	v_add_co_u32_e32 v2, vcc, s74, v2
	v_cvt_pk_bf16_f32 v4, v54, v55
	v_cvt_pk_bf16_f32 v5, v56, v57
	v_cvt_pk_bf16_f32 v6, v46, v47
	v_cvt_pk_bf16_f32 v7, v48, v49
	s_nop 1
	v_addc_co_u32_e32 v3, vcc, 0, v3, vcc
	s_and_b64 vcc, exec, s[0:1]
	s_mov_b64 s[0:1], -1
	global_store_dwordx4 v[2:3], v[4:7], off
	v_cvt_pk_bf16_f32 v2, v38, v39
	v_cvt_pk_bf16_f32 v3, v40, v41
	s_nop 1
	v_cvt_pk_bf16_f32 v4, v34, v35
	v_cvt_pk_bf16_f32 v5, v36, v37
	global_store_dwordx4 v[8:9], v[2:5], off offset:256
	s_cbranch_vccnz .LBB0_1560
	s_andn2_b64 vcc, exec, s[18:19]
	s_cbranch_vccnz .LBB0_1559
	s_barrier
	s_branch .LBB0_1559
